# nt on the 56 wide stores of P0 (weight conversion outputs, normalized fp8 activations, bf16 stream): less dirty L2 to write back at the first grid barrier
# speedup vs baseline: 1.0013x; 1.0013x over previous
; #define LAS __attribute__((address_space(3)))
; #define LDS_WAIT() asm volatile("s_waitcnt lgkmcnt(0)" ::: "memory")
; __device__ __forceinline__ void cvt_item8(const float* __restrict__ src, int K, int N, unsigned char* dst, int kb, int nb, int drow0, float wscale, LAS float* scr, int lane) {
;     const int k0 = kb * 64, n0 = nb * 64;
;     const float* s = src + (size_t)(k0 + (lane >> 4)) * N + n0 + 4 * (lane & 15);
;     f32x4 v[16];
; #pragma unroll
;     for (int i = 0; i < 16; ++i) v[i] = *(const f32x4*)(s + (size_t)(4 * i) * N);
; #pragma unroll
;     for (int i = 0; i < 16; ++i) { LAS float* p = scr + (4 * i + (lane >> 4)) * 65 + 4 * (lane & 15); p[0] = v[i].x * wscale; p[1] = v[i].y * wscale; p[2] = v[i].z * wscale; p[3] = v[i].w * wscale; }
;     LDS_WAIT();
; __device__ __forceinline__ void cvt_dense8(const float* w, int K, int N, unsigned char* dst, LAS float* scr, int gw, int NGW, int lane) {
;     const int nnb = N / 64, items = (K / 64) * nnb;
;     for (int it = gw; it < items; it += NGW) cvt_item8(w, K, N, dst, it / nnb, it % nnb, (it % nnb) * 64, 64.f, scr, lane);
; }
.LBB0_10:
	s_mul_hi_i32 s2, s23, 0x38e38e39
	s_lshr_b32 s3, s2, 31
	s_ashr_i32 s2, s2, 3
	s_add_i32 s2, s2, s3
	s_mul_i32 s3, s2, 0xfffff700
	s_lshl_b32 s2, s2, 6
	s_add_i32 s24, s0, s3
	v_or_b32_e32 v24, s2, v1
	s_movk_i32 s25, 0x2400
	v_mad_i64_i32 v[24:25], s[26:27], v24, s25, v[22:23]
	s_ashr_i32 s25, s24, 31
	s_ashr_i32 s3, s2, 31
	v_lshl_add_u64 v[24:25], s[24:25], 2, v[24:25]
	v_lshl_add_u64 v[30:31], v[20:21], 0, s[2:3]
	v_lshl_add_u64 v[136:137], v[24:25], 0, v[18:19]
	s_mov_b32 s2, 0x9000
	v_add_co_u32_e32 v78, vcc, s2, v136
	v_add_u32_e32 v26, s24, v32
	s_mov_b64 s[2:3], vcc
	s_mov_b32 s24, 0x12000
	v_add_co_u32_e32 v80, vcc, s24, v136
	v_addc_co_u32_e64 v79, s[2:3], 0, v137, s[2:3]
	s_mov_b64 s[2:3], vcc
	s_mov_b32 s24, 0x1b000
	v_add_co_u32_e32 v82, vcc, s24, v136
	v_addc_co_u32_e64 v81, s[2:3], 0, v137, s[2:3]
	s_mov_b64 s[2:3], vcc
	s_mov_b32 s24, 0x24000
	v_add_co_u32_e32 v86, vcc, s24, v136
	v_addc_co_u32_e64 v83, s[2:3], 0, v137, s[2:3]
	s_mov_b64 s[2:3], vcc
	s_mov_b32 s24, 0x2d000
	v_add_co_u32_e32 v90, vcc, s24, v136
	v_addc_co_u32_e64 v87, s[2:3], 0, v137, s[2:3]
	s_mov_b64 s[2:3], vcc
	v_add_co_u32_e32 v94, vcc, s5, v136
	v_addc_co_u32_e64 v91, s[2:3], 0, v137, s[2:3]
	s_mov_b64 s[2:3], vcc
	v_add_co_u32_e32 v98, vcc, s8, v136
	v_addc_co_u32_e64 v95, s[2:3], 0, v137, s[2:3]
	v_add_u32_e32 v28, 16, v26
	v_add_u32_e32 v74, 32, v26
	v_add_u32_e32 v76, 48, v26
	s_mov_b64 s[2:3], vcc
	v_ashrrev_i32_e32 v27, 31, v26
	v_ashrrev_i32_e32 v29, 31, v28
	v_ashrrev_i32_e32 v75, 31, v74
	v_ashrrev_i32_e32 v77, 31, v76
	v_add_co_u32_e32 v102, vcc, s9, v136
	v_addc_co_u32_e64 v99, s[2:3], 0, v137, s[2:3]
	v_lshlrev_b64 v[24:25], 10, v[26:27]
	global_load_dwordx4 v[70:73], v[136:137], off
	v_lshlrev_b64 v[26:27], 10, v[28:29]
	v_lshlrev_b64 v[28:29], 10, v[74:75]
	v_lshlrev_b64 v[74:75], 10, v[76:77]
	s_mov_b64 s[2:3], vcc
	v_lshl_add_u64 v[24:25], v[30:31], 0, v[24:25]
	v_lshl_add_u64 v[26:27], v[30:31], 0, v[26:27]
	v_lshl_add_u64 v[28:29], v[30:31], 0, v[28:29]
	v_lshl_add_u64 v[30:31], v[30:31], 0, v[74:75]
	global_load_dwordx4 v[74:77], v[78:79], off
	v_add_co_u32_e32 v106, vcc, s10, v136
	v_addc_co_u32_e64 v103, s[2:3], 0, v137, s[2:3]
	global_load_dwordx4 v[82:85], v[82:83], off
	s_mov_b64 s[2:3], vcc
	global_load_dwordx4 v[78:81], v[80:81], off
	v_add_co_u32_e32 v110, vcc, s11, v136
	v_addc_co_u32_e64 v107, s[2:3], 0, v137, s[2:3]
	global_load_dwordx4 v[86:89], v[86:87], off
	s_mov_b64 s[2:3], vcc
	global_load_dwordx4 v[90:93], v[90:91], off
	v_add_co_u32_e32 v114, vcc, s18, v136
	v_addc_co_u32_e64 v111, s[2:3], 0, v137, s[2:3]
	global_load_dwordx4 v[94:97], v[94:95], off
	s_mov_b64 s[2:3], vcc
	global_load_dwordx4 v[98:101], v[98:99], off
	v_add_co_u32_e32 v118, vcc, s19, v136
	v_addc_co_u32_e64 v115, s[2:3], 0, v137, s[2:3]
	global_load_dwordx4 v[102:105], v[102:103], off
	s_mov_b64 s[2:3], vcc
	global_load_dwordx4 v[106:109], v[106:107], off
	v_add_co_u32_e32 v122, vcc, s20, v136
	v_addc_co_u32_e64 v119, s[2:3], 0, v137, s[2:3]
	global_load_dwordx4 v[110:113], v[110:111], off
	s_mov_b64 s[2:3], vcc
	global_load_dwordx4 v[114:117], v[114:115], off
	v_add_co_u32_e32 v126, vcc, s21, v136
	v_addc_co_u32_e64 v123, s[2:3], 0, v137, s[2:3]
	global_load_dwordx4 v[118:121], v[118:119], off
	s_mov_b64 s[2:3], vcc
	global_load_dwordx4 v[122:125], v[122:123], off
	v_add_co_u32_e32 v136, vcc, s22, v136
	v_addc_co_u32_e64 v127, s[2:3], 0, v137, s[2:3]
	global_load_dwordx4 v[126:129], v[126:127], off
	v_addc_co_u32_e32 v137, vcc, 0, v137, vcc
	global_load_dwordx4 v[136:139], v[136:137], off
	v_mov_b32_e32 v2, 0
	v_mov_b32_e32 v3, 0
	v_mov_b32_e32 v4, 0
	v_mov_b32_e32 v5, 0
	v_mov_b32_e32 v6, 0
	v_mov_b32_e32 v7, 0
	v_mov_b32_e32 v8, 0
	v_mov_b32_e32 v9, 0
	v_mov_b32_e32 v10, 0
	v_mov_b32_e32 v11, 0
	v_mov_b32_e32 v12, 0
	v_mov_b32_e32 v13, 0
	v_mov_b32_e32 v14, 0
	v_mov_b32_e32 v15, 0
	v_mov_b32_e32 v16, 0
	v_mov_b32_e32 v17, 0
	s_add_i32 s23, s23, s28
	s_add_i32 s0, s0, s1
	s_cmpk_lt_i32 s23, 0x240
	s_waitcnt vmcnt(15)
	v_pk_mul_f32 v[70:71], v[70:71], s[4:5] op_sel_hi:[1,0]
	v_pk_mul_f32 v[72:73], v[72:73], s[4:5] op_sel_hi:[1,0]
	ds_write2_b32 v35, v70, v71 offset1:1
	ds_write2_b32 v35, v72, v73 offset0:2 offset1:3
	s_waitcnt vmcnt(14)
	v_pk_mul_f32 v[70:71], v[74:75], s[4:5] op_sel_hi:[1,0]
	v_pk_mul_f32 v[72:73], v[76:77], s[4:5] op_sel_hi:[1,0]
	ds_write2_b32 v36, v70, v71 offset1:1
	ds_write2_b32 v37, v72, v73 offset1:1
	s_waitcnt vmcnt(12)
	v_pk_mul_f32 v[70:71], v[78:79], s[4:5] op_sel_hi:[1,0]
	v_pk_mul_f32 v[72:73], v[80:81], s[4:5] op_sel_hi:[1,0]
	ds_write2_b32 v38, v70, v71 offset1:1
	ds_write2_b32 v39, v72, v73 offset1:1
	v_pk_mul_f32 v[70:71], v[82:83], s[4:5] op_sel_hi:[1,0]
	v_pk_mul_f32 v[72:73], v[84:85], s[4:5] op_sel_hi:[1,0]
	ds_write2_b32 v40, v70, v71 offset1:1
	ds_write2_b32 v41, v72, v73 offset1:1
	s_waitcnt vmcnt(11)
	v_pk_mul_f32 v[70:71], v[86:87], s[4:5] op_sel_hi:[1,0]
	v_pk_mul_f32 v[72:73], v[88:89], s[4:5] op_sel_hi:[1,0]
	ds_write2_b32 v42, v70, v71 offset1:1
	ds_write2_b32 v43, v72, v73 offset1:1
	s_waitcnt vmcnt(10)
	v_pk_mul_f32 v[70:71], v[90:91], s[4:5] op_sel_hi:[1,0]
	v_pk_mul_f32 v[72:73], v[92:93], s[4:5] op_sel_hi:[1,0]
	ds_write2_b32 v44, v70, v71 offset1:1
	ds_write2_b32 v45, v72, v73 offset1:1
	s_waitcnt vmcnt(9)
	v_pk_mul_f32 v[70:71], v[94:95], s[4:5] op_sel_hi:[1,0]
	v_pk_mul_f32 v[72:73], v[96:97], s[4:5] op_sel_hi:[1,0]
	ds_write2_b32 v46, v70, v71 offset1:1
	ds_write2_b32 v47, v72, v73 offset1:1
	s_waitcnt vmcnt(8)
; __device__ __forceinline__ unsigned pk4_fp8(float a, float b, float c, float d) { unsigned w = 0u; w = __builtin_amdgcn_cvt_pk_fp8_f32(a, b, w, false); w = __builtin_amdgcn_cvt_pk_fp8_f32(c, d, w, true); return w; }
; #define LAS __attribute__((address_space(3)))
; #define LDS_WAIT() asm volatile("s_waitcnt lgkmcnt(0)" ::: "memory")
; __device__ __forceinline__ void cvt_item8(const float* __restrict__ src, int K, int N, unsigned char* dst, int kb, int nb, int drow0, float wscale, LAS float* scr, int lane) {
;     ...
;     LDS_WAIT();
;     const int c = lane & 3;
; #pragma unroll
;     for (int j = 0; j < 4; ++j) { const int n = (lane >> 2) + 16 * j; const LAS float* q = scr + (16 * c) * 65 + n;
;         v4u o; o.x = pg8::pk4_fp8(q[0], q[65], q[130], q[195]); o.y = pg8::pk4_fp8(q[260], q[325], q[390], q[455]);
;         o.z = pg8::pk4_fp8(q[520], q[585], q[650], q[715]); o.w = pg8::pk4_fp8(q[780], q[845], q[910], q[975]);
;         *(v4u*)(dst + (size_t)(drow0 + n) * K + k0 + 16 * c) = o; }
;     LDS_WAIT();
	v_pk_mul_f32 v[70:71], v[98:99], s[4:5] op_sel_hi:[1,0]
	v_pk_mul_f32 v[72:73], v[100:101], s[4:5] op_sel_hi:[1,0]
	ds_write2_b32 v48, v70, v71 offset1:1
	ds_write2_b32 v49, v72, v73 offset1:1
	s_waitcnt vmcnt(7)
	v_pk_mul_f32 v[70:71], v[102:103], s[4:5] op_sel_hi:[1,0]
	v_pk_mul_f32 v[72:73], v[104:105], s[4:5] op_sel_hi:[1,0]
	ds_write2_b32 v50, v70, v71 offset1:1
	ds_write2_b32 v51, v72, v73 offset1:1
	s_waitcnt vmcnt(6)
	v_pk_mul_f32 v[70:71], v[106:107], s[4:5] op_sel_hi:[1,0]
	v_pk_mul_f32 v[72:73], v[108:109], s[4:5] op_sel_hi:[1,0]
	ds_write2_b32 v52, v70, v71 offset1:1
	ds_write2_b32 v53, v72, v73 offset1:1
	s_waitcnt vmcnt(5)
	v_pk_mul_f32 v[70:71], v[110:111], s[4:5] op_sel_hi:[1,0]
	v_pk_mul_f32 v[72:73], v[112:113], s[4:5] op_sel_hi:[1,0]
	ds_write2_b32 v54, v70, v71 offset1:1
	ds_write2_b32 v55, v72, v73 offset1:1
	s_waitcnt vmcnt(4)
	v_pk_mul_f32 v[70:71], v[114:115], s[4:5] op_sel_hi:[1,0]
	v_pk_mul_f32 v[72:73], v[116:117], s[4:5] op_sel_hi:[1,0]
	ds_write2_b32 v56, v70, v71 offset1:1
	ds_write2_b32 v57, v72, v73 offset1:1
	s_waitcnt vmcnt(3)
	v_pk_mul_f32 v[70:71], v[118:119], s[4:5] op_sel_hi:[1,0]
	v_pk_mul_f32 v[72:73], v[120:121], s[4:5] op_sel_hi:[1,0]
	ds_write2_b32 v58, v70, v71 offset1:1
	ds_write2_b32 v59, v72, v73 offset1:1
	s_waitcnt vmcnt(2)
	v_pk_mul_f32 v[70:71], v[122:123], s[4:5] op_sel_hi:[1,0]
	v_pk_mul_f32 v[72:73], v[124:125], s[4:5] op_sel_hi:[1,0]
	ds_write2_b32 v60, v70, v71 offset1:1
	ds_write2_b32 v61, v72, v73 offset1:1
	s_waitcnt vmcnt(1)
	v_pk_mul_f32 v[70:71], v[126:127], s[4:5] op_sel_hi:[1,0]
	v_pk_mul_f32 v[72:73], v[128:129], s[4:5] op_sel_hi:[1,0]
	ds_write2_b32 v62, v70, v71 offset1:1
	ds_write2_b32 v63, v72, v73 offset1:1
	s_waitcnt vmcnt(0)
	v_pk_mul_f32 v[70:71], v[136:137], s[4:5] op_sel_hi:[1,0]
	v_pk_mul_f32 v[72:73], v[138:139], s[4:5] op_sel_hi:[1,0]
	ds_write2_b32 v64, v70, v71 offset1:1
	ds_write2_b32 v65, v72, v73 offset1:1
	s_waitcnt lgkmcnt(0)
	ds_read2_b32 v[70:71], v34 offset1:16
	ds_read2_b32 v[72:73], v34 offset0:65 offset1:81
	ds_read2_b32 v[74:75], v66 offset0:4 offset1:20
	ds_read2_b32 v[76:77], v66 offset0:69 offset1:85
	ds_read2_b32 v[78:79], v67 offset0:8 offset1:24
	ds_read2_b32 v[80:81], v67 offset0:73 offset1:89
	ds_read2_b32 v[82:83], v68 offset0:12 offset1:28
	ds_read2_b32 v[84:85], v68 offset0:77 offset1:93
	ds_read2_b32 v[86:87], v34 offset0:32 offset1:48
	ds_read2_b32 v[88:89], v34 offset0:97 offset1:113
	ds_read2_b32 v[90:91], v66 offset0:36 offset1:52
	ds_read2_b32 v[92:93], v66 offset0:101 offset1:117
	ds_read2_b32 v[94:95], v67 offset0:40 offset1:56
	ds_read2_b32 v[96:97], v67 offset0:105 offset1:121
	ds_read2_b32 v[98:99], v68 offset0:44 offset1:60
	ds_read2_b32 v[100:101], v68 offset0:109 offset1:125
	ds_read2_b32 v[102:103], v34 offset0:130 offset1:146
	ds_read2_b32 v[104:105], v34 offset0:195 offset1:211
	ds_read2_b32 v[106:107], v66 offset0:134 offset1:150
	ds_read2_b32 v[108:109], v66 offset0:199 offset1:215
	ds_read2_b32 v[110:111], v67 offset0:138 offset1:154
	ds_read2_b32 v[112:113], v67 offset0:203 offset1:219
	ds_read2_b32 v[114:115], v68 offset0:142 offset1:158
	ds_read2_b32 v[116:117], v68 offset0:207 offset1:223
	ds_read2_b32 v[118:119], v34 offset0:162 offset1:178
	ds_read2_b32 v[120:121], v34 offset0:227 offset1:243
	ds_read2_b32 v[122:123], v66 offset0:166 offset1:182
	ds_read2_b32 v[124:125], v66 offset0:231 offset1:247
	ds_read2_b32 v[126:127], v67 offset0:170 offset1:186
	ds_read2_b32 v[128:129], v67 offset0:235 offset1:251
	ds_read2_b32 v[136:137], v68 offset0:174 offset1:190
	ds_read2_b32 v[138:139], v68 offset0:239 offset1:255
	s_waitcnt lgkmcnt(14)
	v_cvt_pk_fp8_f32 v2, v70, v72
	v_cvt_pk_fp8_f32 v3, v74, v76
	v_cvt_pk_fp8_f32 v4, v78, v80
	v_cvt_pk_fp8_f32 v5, v82, v84
	v_cvt_pk_fp8_f32 v6, v71, v73
	v_cvt_pk_fp8_f32 v7, v75, v77
	v_cvt_pk_fp8_f32 v8, v79, v81
	v_cvt_pk_fp8_f32 v9, v83, v85
	v_cvt_pk_fp8_f32 v10, v86, v88
	v_cvt_pk_fp8_f32 v11, v90, v92
	v_cvt_pk_fp8_f32 v12, v94, v96
	v_cvt_pk_fp8_f32 v13, v98, v100
	v_cvt_pk_fp8_f32 v14, v87, v89
	v_cvt_pk_fp8_f32 v15, v91, v93
	v_cvt_pk_fp8_f32 v16, v95, v97
	v_cvt_pk_fp8_f32 v17, v99, v101
	v_cvt_pk_fp8_f32 v2, v102, v104 op_sel:[0,0,1]
	s_waitcnt lgkmcnt(12)
	v_cvt_pk_fp8_f32 v3, v106, v108 op_sel:[0,0,1]
	s_waitcnt lgkmcnt(10)
	v_cvt_pk_fp8_f32 v4, v110, v112 op_sel:[0,0,1]
	s_waitcnt lgkmcnt(8)
	v_cvt_pk_fp8_f32 v5, v114, v116 op_sel:[0,0,1]
	v_cvt_pk_fp8_f32 v6, v103, v105 op_sel:[0,0,1]
	v_cvt_pk_fp8_f32 v7, v107, v109 op_sel:[0,0,1]
	v_cvt_pk_fp8_f32 v8, v111, v113 op_sel:[0,0,1]
	v_cvt_pk_fp8_f32 v9, v115, v117 op_sel:[0,0,1]
	s_waitcnt lgkmcnt(6)
	v_cvt_pk_fp8_f32 v10, v118, v120 op_sel:[0,0,1]
	s_waitcnt lgkmcnt(4)
	v_cvt_pk_fp8_f32 v11, v122, v124 op_sel:[0,0,1]
	s_waitcnt lgkmcnt(2)
	v_cvt_pk_fp8_f32 v12, v126, v128 op_sel:[0,0,1]
	s_waitcnt lgkmcnt(0)
	v_cvt_pk_fp8_f32 v13, v136, v138 op_sel:[0,0,1]
	v_cvt_pk_fp8_f32 v14, v119, v121 op_sel:[0,0,1]
	v_cvt_pk_fp8_f32 v15, v123, v125 op_sel:[0,0,1]
	v_cvt_pk_fp8_f32 v16, v127, v129 op_sel:[0,0,1]
	v_cvt_pk_fp8_f32 v17, v137, v139 op_sel:[0,0,1]
	global_store_dwordx4 v[24:25], v[2:5], off nt
	global_store_dwordx4 v[26:27], v[6:9], off nt
	global_store_dwordx4 v[28:29], v[10:13], off nt
	global_store_dwordx4 v[30:31], v[14:17], off nt
	s_waitcnt lgkmcnt(0)
	s_cbranch_scc1 .LBB0_10

; #define LAS __attribute__((address_space(3)))
; #define LDS_WAIT() asm volatile("s_waitcnt lgkmcnt(0)" ::: "memory")
; __device__ __forceinline__ void cvt_item8(const float* __restrict__ src, int K, int N, unsigned char* dst, int kb, int nb, int drow0, float wscale, LAS float* scr, int lane) {
;     const int k0 = kb * 64, n0 = nb * 64;
;     const float* s = src + (size_t)(k0 + (lane >> 4)) * N + n0 + 4 * (lane & 15);
;     f32x4 v[16];
; #pragma unroll
;     for (int i = 0; i < 16; ++i) v[i] = *(const f32x4*)(s + (size_t)(4 * i) * N);
; #pragma unroll
;     for (int i = 0; i < 16; ++i) { LAS float* p = scr + (4 * i + (lane >> 4)) * 65 + 4 * (lane & 15); p[0] = v[i].x * wscale; p[1] = v[i].y * wscale; p[2] = v[i].z * wscale; p[3] = v[i].w * wscale; }
;     LDS_WAIT();
; __device__ __forceinline__ void cvt_dense8(const float* w, int K, int N, unsigned char* dst, LAS float* scr, int gw, int NGW, int lane) {
;     const int nnb = N / 64, items = (K / 64) * nnb;
;     for (int it = gw; it < items; it += NGW) cvt_item8(w, K, N, dst, it / nnb, it % nnb, (it % nnb) * 64, 64.f, scr, lane);
; }
.LBB0_13:
	s_ashr_i32 s23, s22, 31
	s_lshr_b32 s23, s23, 28
	s_add_i32 s23, s22, s23
	s_ashr_i32 s23, s23, 4
	s_lshl_b32 s24, s23, 6
	v_or_b32_e32 v22, s24, v1
	s_lshl_b32 s25, s23, 10
	v_ashrrev_i32_e32 v23, 31, v22
	s_sub_i32 s26, s0, s25
	v_lshlrev_b64 v[22:23], 12, v[22:23]
	s_ashr_i32 s27, s26, 31
	v_lshl_add_u64 v[22:23], s[76:77], 0, v[22:23]
	v_lshl_add_u64 v[72:73], s[26:27], 2, v[22:23]
	v_lshl_add_u64 v[72:73], v[72:73], 0, v[18:19]
	s_movk_i32 s23, 0x4000
	v_add_co_u32_e32 v74, vcc, s23, v72
	s_mov_b32 s23, 0x8000
	s_nop 0
	v_addc_co_u32_e32 v75, vcc, 0, v73, vcc
	v_add_co_u32_e32 v76, vcc, s23, v72
	s_mov_b32 s23, 0xc000
	s_nop 0
	v_addc_co_u32_e32 v77, vcc, 0, v73, vcc
	v_add_co_u32_e32 v80, vcc, s23, v72
	s_mov_b32 s23, 0x10000
	s_nop 0
	v_addc_co_u32_e32 v81, vcc, 0, v73, vcc
	v_add_co_u32_e32 v84, vcc, s23, v72
	s_mov_b32 s23, 0x14000
	s_nop 0
	v_addc_co_u32_e32 v85, vcc, 0, v73, vcc
	v_add_co_u32_e32 v88, vcc, s23, v72
	s_mov_b32 s23, 0x18000
	s_nop 0
	v_addc_co_u32_e32 v89, vcc, 0, v73, vcc
	v_add_co_u32_e32 v92, vcc, s23, v72
	v_add_u32_e32 v24, s26, v32
	s_nop 0
	v_addc_co_u32_e32 v93, vcc, 0, v73, vcc
	v_add_co_u32_e32 v96, vcc, s3, v72
	s_ashr_i32 s25, s24, 31
	s_nop 0
	v_addc_co_u32_e32 v97, vcc, 0, v73, vcc
	v_add_co_u32_e32 v100, vcc, s8, v72
	v_ashrrev_i32_e32 v25, 31, v24
	s_nop 0
	v_addc_co_u32_e32 v101, vcc, 0, v73, vcc
	v_add_co_u32_e32 v104, vcc, s9, v72
	v_add_u32_e32 v26, 16, v24
	s_nop 0
	v_addc_co_u32_e32 v105, vcc, 0, v73, vcc
	v_add_co_u32_e32 v108, vcc, s10, v72
	v_add_u32_e32 v68, 32, v24
	s_nop 0
	v_addc_co_u32_e32 v109, vcc, 0, v73, vcc
	v_add_co_u32_e32 v112, vcc, s11, v72
	v_add_u32_e32 v70, 48, v24
	s_nop 0
	v_addc_co_u32_e32 v113, vcc, 0, v73, vcc
	v_add_co_u32_e32 v116, vcc, s18, v72
	v_lshl_add_u64 v[28:29], v[20:21], 0, s[24:25]
	s_nop 0
	v_addc_co_u32_e32 v117, vcc, 0, v73, vcc
	v_add_co_u32_e32 v120, vcc, s19, v72
	v_lshlrev_b64 v[24:25], 10, v[24:25]
	v_ashrrev_i32_e32 v27, 31, v26
	v_ashrrev_i32_e32 v69, 31, v68
	v_ashrrev_i32_e32 v71, 31, v70
	v_addc_co_u32_e32 v121, vcc, 0, v73, vcc
	v_lshl_add_u64 v[22:23], v[28:29], 0, v[24:25]
	v_lshlrev_b64 v[24:25], 10, v[26:27]
	v_lshlrev_b64 v[26:27], 10, v[68:69]
	v_lshlrev_b64 v[68:69], 10, v[70:71]
	v_add_co_u32_e32 v124, vcc, s20, v72
	v_lshl_add_u64 v[24:25], v[28:29], 0, v[24:25]
	v_lshl_add_u64 v[26:27], v[28:29], 0, v[26:27]
	v_lshl_add_u64 v[28:29], v[28:29], 0, v[68:69]
	global_load_dwordx4 v[68:71], v[72:73], off
	v_addc_co_u32_e32 v125, vcc, 0, v73, vcc
	v_add_co_u32_e32 v128, vcc, s21, v72
	v_mov_b32_e32 v2, 0
	s_nop 0
	v_addc_co_u32_e32 v129, vcc, 0, v73, vcc
	global_load_dwordx4 v[72:75], v[74:75], off
	s_nop 0
	global_load_dwordx4 v[76:79], v[76:77], off
	s_nop 0
	global_load_dwordx4 v[80:83], v[80:81], off
	s_nop 0
	global_load_dwordx4 v[84:87], v[84:85], off
	s_nop 0
	global_load_dwordx4 v[88:91], v[88:89], off
	s_nop 0
	global_load_dwordx4 v[92:95], v[92:93], off
	s_nop 0
	global_load_dwordx4 v[96:99], v[96:97], off
	s_nop 0
	global_load_dwordx4 v[100:103], v[100:101], off
	s_nop 0
	global_load_dwordx4 v[104:107], v[104:105], off
	s_nop 0
	global_load_dwordx4 v[108:111], v[108:109], off
	s_nop 0
	global_load_dwordx4 v[112:115], v[112:113], off
	s_nop 0
	global_load_dwordx4 v[116:119], v[116:117], off
	s_nop 0
	global_load_dwordx4 v[120:123], v[120:121], off
	s_nop 0
	global_load_dwordx4 v[124:127], v[124:125], off
	s_nop 0
	global_load_dwordx4 v[136:139], v[128:129], off
	v_mov_b32_e32 v3, 0
	v_mov_b32_e32 v4, 0
	v_mov_b32_e32 v5, 0
	v_mov_b32_e32 v6, 0
	v_mov_b32_e32 v7, 0
	v_mov_b32_e32 v8, 0
	v_mov_b32_e32 v9, 0
	v_mov_b32_e32 v10, 0
	v_mov_b32_e32 v11, 0
	v_mov_b32_e32 v12, 0
	v_mov_b32_e32 v13, 0
	v_mov_b32_e32 v14, 0
	v_mov_b32_e32 v15, 0
	v_mov_b32_e32 v16, 0
	v_mov_b32_e32 v17, 0
	s_add_i32 s22, s22, s28
	s_add_i32 s0, s0, s1
	s_cmpk_lt_i32 s22, 0x100
	s_waitcnt vmcnt(15)
	v_pk_mul_f32 v[68:69], v[68:69], s[2:3] op_sel_hi:[1,0]
	v_pk_mul_f32 v[70:71], v[70:71], s[2:3] op_sel_hi:[1,0]
	ds_write2_b32 v31, v68, v69 offset1:1
	ds_write2_b32 v31, v70, v71 offset0:2 offset1:3
	s_waitcnt vmcnt(14)
	v_pk_mul_f32 v[68:69], v[72:73], s[2:3] op_sel_hi:[1,0]
	v_pk_mul_f32 v[70:71], v[74:75], s[2:3] op_sel_hi:[1,0]
	s_waitcnt vmcnt(13)
	v_pk_mul_f32 v[72:73], v[76:77], s[2:3] op_sel_hi:[1,0]
	v_pk_mul_f32 v[74:75], v[78:79], s[2:3] op_sel_hi:[1,0]
	s_waitcnt vmcnt(12)
	v_pk_mul_f32 v[76:77], v[80:81], s[2:3] op_sel_hi:[1,0]
	v_pk_mul_f32 v[78:79], v[82:83], s[2:3] op_sel_hi:[1,0]
	s_waitcnt vmcnt(11)
	v_pk_mul_f32 v[80:81], v[84:85], s[2:3] op_sel_hi:[1,0]
	v_pk_mul_f32 v[82:83], v[86:87], s[2:3] op_sel_hi:[1,0]
	s_waitcnt vmcnt(10)
	v_pk_mul_f32 v[84:85], v[88:89], s[2:3] op_sel_hi:[1,0]
	v_pk_mul_f32 v[86:87], v[90:91], s[2:3] op_sel_hi:[1,0]
	s_waitcnt vmcnt(9)
	v_pk_mul_f32 v[88:89], v[92:93], s[2:3] op_sel_hi:[1,0]
	v_pk_mul_f32 v[90:91], v[94:95], s[2:3] op_sel_hi:[1,0]
	s_waitcnt vmcnt(8)
	v_pk_mul_f32 v[92:93], v[96:97], s[2:3] op_sel_hi:[1,0]
	v_pk_mul_f32 v[94:95], v[98:99], s[2:3] op_sel_hi:[1,0]
	s_waitcnt vmcnt(7)
	v_pk_mul_f32 v[96:97], v[100:101], s[2:3] op_sel_hi:[1,0]
	v_pk_mul_f32 v[98:99], v[102:103], s[2:3] op_sel_hi:[1,0]
	s_waitcnt vmcnt(6)
	v_pk_mul_f32 v[100:101], v[104:105], s[2:3] op_sel_hi:[1,0]
	v_pk_mul_f32 v[102:103], v[106:107], s[2:3] op_sel_hi:[1,0]
	s_waitcnt vmcnt(5)
; __device__ __forceinline__ unsigned pk4_fp8(float a, float b, float c, float d) { unsigned w = 0u; w = __builtin_amdgcn_cvt_pk_fp8_f32(a, b, w, false); w = __builtin_amdgcn_cvt_pk_fp8_f32(c, d, w, true); return w; }
; #define LAS __attribute__((address_space(3)))
; #define LDS_WAIT() asm volatile("s_waitcnt lgkmcnt(0)" ::: "memory")
; __device__ __forceinline__ void cvt_item8(const float* __restrict__ src, int K, int N, unsigned char* dst, int kb, int nb, int drow0, float wscale, LAS float* scr, int lane) {
;     ...
;     LDS_WAIT();
;     const int c = lane & 3;
; #pragma unroll
;     for (int j = 0; j < 4; ++j) { const int n = (lane >> 2) + 16 * j; const LAS float* q = scr + (16 * c) * 65 + n;
;         v4u o; o.x = pg8::pk4_fp8(q[0], q[65], q[130], q[195]); o.y = pg8::pk4_fp8(q[260], q[325], q[390], q[455]);
;         o.z = pg8::pk4_fp8(q[520], q[585], q[650], q[715]); o.w = pg8::pk4_fp8(q[780], q[845], q[910], q[975]);
;         *(v4u*)(dst + (size_t)(drow0 + n) * K + k0 + 16 * c) = o; }
;     LDS_WAIT();
	v_pk_mul_f32 v[104:105], v[108:109], s[2:3] op_sel_hi:[1,0]
	v_pk_mul_f32 v[106:107], v[110:111], s[2:3] op_sel_hi:[1,0]
	s_waitcnt vmcnt(4)
	v_pk_mul_f32 v[108:109], v[112:113], s[2:3] op_sel_hi:[1,0]
	v_pk_mul_f32 v[110:111], v[114:115], s[2:3] op_sel_hi:[1,0]
	s_waitcnt vmcnt(3)
	v_pk_mul_f32 v[112:113], v[116:117], s[2:3] op_sel_hi:[1,0]
	v_pk_mul_f32 v[114:115], v[118:119], s[2:3] op_sel_hi:[1,0]
	s_waitcnt vmcnt(2)
	v_pk_mul_f32 v[116:117], v[120:121], s[2:3] op_sel_hi:[1,0]
	v_pk_mul_f32 v[118:119], v[122:123], s[2:3] op_sel_hi:[1,0]
	s_waitcnt vmcnt(1)
	v_pk_mul_f32 v[120:121], v[124:125], s[2:3] op_sel_hi:[1,0]
	v_pk_mul_f32 v[122:123], v[126:127], s[2:3] op_sel_hi:[1,0]
	s_waitcnt vmcnt(0)
	v_pk_mul_f32 v[124:125], v[136:137], s[2:3] op_sel_hi:[1,0]
	v_pk_mul_f32 v[126:127], v[138:139], s[2:3] op_sel_hi:[1,0]
	ds_write2_b32 v34, v68, v69 offset1:1
	ds_write2_b32 v35, v70, v71 offset1:1
	ds_write2_b32 v36, v72, v73 offset1:1
	ds_write2_b32 v37, v74, v75 offset1:1
	ds_write2_b32 v38, v76, v77 offset1:1
	ds_write2_b32 v39, v78, v79 offset1:1
	ds_write2_b32 v40, v80, v81 offset1:1
	ds_write2_b32 v41, v82, v83 offset1:1
	ds_write2_b32 v42, v84, v85 offset1:1
	ds_write2_b32 v43, v86, v87 offset1:1
	ds_write2_b32 v44, v88, v89 offset1:1
	ds_write2_b32 v45, v90, v91 offset1:1
	ds_write2_b32 v46, v92, v93 offset1:1
	ds_write2_b32 v47, v94, v95 offset1:1
	ds_write2_b32 v48, v96, v97 offset1:1
	ds_write2_b32 v49, v98, v99 offset1:1
	ds_write2_b32 v50, v100, v101 offset1:1
	ds_write2_b32 v51, v102, v103 offset1:1
	ds_write2_b32 v52, v104, v105 offset1:1
	ds_write2_b32 v53, v106, v107 offset1:1
	ds_write2_b32 v54, v108, v109 offset1:1
	ds_write2_b32 v55, v110, v111 offset1:1
	ds_write2_b32 v56, v112, v113 offset1:1
	ds_write2_b32 v57, v114, v115 offset1:1
	ds_write2_b32 v58, v116, v117 offset1:1
	ds_write2_b32 v59, v118, v119 offset1:1
	ds_write2_b32 v60, v120, v121 offset1:1
	ds_write2_b32 v61, v122, v123 offset1:1
	ds_write2_b32 v62, v124, v125 offset1:1
	ds_write2_b32 v63, v126, v127 offset1:1
	s_waitcnt lgkmcnt(0)
	ds_read2_b32 v[68:69], v30 offset1:16
	ds_read2_b32 v[70:71], v30 offset0:65 offset1:81
	ds_read2_b32 v[72:73], v30 offset0:130 offset1:146
	ds_read2_b32 v[74:75], v30 offset0:195 offset1:211
	ds_read2_b32 v[76:77], v64 offset0:4 offset1:20
	ds_read2_b32 v[78:79], v64 offset0:69 offset1:85
	ds_read2_b32 v[80:81], v64 offset0:134 offset1:150
	ds_read2_b32 v[82:83], v64 offset0:199 offset1:215
	ds_read2_b32 v[84:85], v65 offset0:8 offset1:24
	ds_read2_b32 v[86:87], v65 offset0:73 offset1:89
	ds_read2_b32 v[88:89], v65 offset0:138 offset1:154
	ds_read2_b32 v[90:91], v65 offset0:203 offset1:219
	ds_read2_b32 v[92:93], v66 offset0:12 offset1:28
	ds_read2_b32 v[94:95], v66 offset0:77 offset1:93
	ds_read2_b32 v[96:97], v66 offset0:142 offset1:158
	ds_read2_b32 v[98:99], v66 offset0:207 offset1:223
	ds_read2_b32 v[100:101], v30 offset0:32 offset1:48
	ds_read2_b32 v[102:103], v30 offset0:97 offset1:113
	ds_read2_b32 v[104:105], v30 offset0:162 offset1:178
	ds_read2_b32 v[106:107], v64 offset0:36 offset1:52
	ds_read2_b32 v[108:109], v64 offset0:101 offset1:117
	ds_read2_b32 v[110:111], v65 offset0:40 offset1:56
	ds_read2_b32 v[112:113], v65 offset0:105 offset1:121
	ds_read2_b32 v[114:115], v66 offset0:44 offset1:60
	ds_read2_b32 v[116:117], v66 offset0:109 offset1:125
	ds_read2_b32 v[118:119], v30 offset0:227 offset1:243
	ds_read2_b32 v[120:121], v64 offset0:166 offset1:182
	ds_read2_b32 v[122:123], v64 offset0:231 offset1:247
	ds_read2_b32 v[124:125], v65 offset0:170 offset1:186
	ds_read2_b32 v[126:127], v65 offset0:235 offset1:251
	ds_read2_b32 v[128:129], v66 offset0:174 offset1:190
	ds_read2_b32 v[136:137], v66 offset0:239 offset1:255
	s_waitcnt lgkmcnt(14)
	v_cvt_pk_fp8_f32 v2, v68, v70
	v_cvt_pk_fp8_f32 v3, v76, v78
	v_cvt_pk_fp8_f32 v4, v84, v86
	v_cvt_pk_fp8_f32 v5, v92, v94
	v_cvt_pk_fp8_f32 v6, v69, v71
	v_cvt_pk_fp8_f32 v7, v77, v79
	v_cvt_pk_fp8_f32 v8, v85, v87
	v_cvt_pk_fp8_f32 v9, v93, v95
	v_cvt_pk_fp8_f32 v10, v100, v102
	s_waitcnt lgkmcnt(11)
	v_cvt_pk_fp8_f32 v11, v106, v108
	s_waitcnt lgkmcnt(9)
	v_cvt_pk_fp8_f32 v12, v110, v112
	s_waitcnt lgkmcnt(7)
	v_cvt_pk_fp8_f32 v13, v114, v116
	v_cvt_pk_fp8_f32 v14, v101, v103
	v_cvt_pk_fp8_f32 v15, v107, v109
	v_cvt_pk_fp8_f32 v16, v111, v113
	v_cvt_pk_fp8_f32 v17, v115, v117
	v_cvt_pk_fp8_f32 v2, v72, v74 op_sel:[0,0,1]
	v_cvt_pk_fp8_f32 v3, v80, v82 op_sel:[0,0,1]
	v_cvt_pk_fp8_f32 v4, v88, v90 op_sel:[0,0,1]
	v_cvt_pk_fp8_f32 v5, v96, v98 op_sel:[0,0,1]
	v_cvt_pk_fp8_f32 v6, v73, v75 op_sel:[0,0,1]
	v_cvt_pk_fp8_f32 v7, v81, v83 op_sel:[0,0,1]
	v_cvt_pk_fp8_f32 v8, v89, v91 op_sel:[0,0,1]
	v_cvt_pk_fp8_f32 v9, v97, v99 op_sel:[0,0,1]
	s_waitcnt lgkmcnt(6)
	v_cvt_pk_fp8_f32 v10, v104, v118 op_sel:[0,0,1]
	s_waitcnt lgkmcnt(4)
	v_cvt_pk_fp8_f32 v11, v120, v122 op_sel:[0,0,1]
	s_waitcnt lgkmcnt(2)
	v_cvt_pk_fp8_f32 v12, v124, v126 op_sel:[0,0,1]
	s_waitcnt lgkmcnt(0)
	v_cvt_pk_fp8_f32 v13, v128, v136 op_sel:[0,0,1]
	v_cvt_pk_fp8_f32 v14, v105, v119 op_sel:[0,0,1]
	v_cvt_pk_fp8_f32 v15, v121, v123 op_sel:[0,0,1]
	v_cvt_pk_fp8_f32 v16, v125, v127 op_sel:[0,0,1]
	v_cvt_pk_fp8_f32 v17, v129, v137 op_sel:[0,0,1]
	global_store_dwordx4 v[22:23], v[2:5], off nt
	global_store_dwordx4 v[24:25], v[6:9], off nt
	global_store_dwordx4 v[26:27], v[10:13], off nt
	global_store_dwordx4 v[28:29], v[14:17], off nt
	s_waitcnt lgkmcnt(0)
	s_cbranch_scc1 .LBB0_13
	v_readlane_b32 s22, v254, 51

; #define LAS __attribute__((address_space(3)))
; #define LDS_WAIT() asm volatile("s_waitcnt lgkmcnt(0)" ::: "memory")
; __device__ __forceinline__ void cvt_item8(const float* __restrict__ src, int K, int N, unsigned char* dst, int kb, int nb, int drow0, float wscale, LAS float* scr, int lane) {
;     const int k0 = kb * 64, n0 = nb * 64;
;     const float* s = src + (size_t)(k0 + (lane >> 4)) * N + n0 + 4 * (lane & 15);
;     f32x4 v[16];
; #pragma unroll
;     for (int i = 0; i < 16; ++i) v[i] = *(const f32x4*)(s + (size_t)(4 * i) * N);
; #pragma unroll
;     for (int i = 0; i < 16; ++i) { LAS float* p = scr + (4 * i + (lane >> 4)) * 65 + 4 * (lane & 15); p[0] = v[i].x * wscale; p[1] = v[i].y * wscale; p[2] = v[i].z * wscale; p[3] = v[i].w * wscale; }
;     LDS_WAIT();
; __device__ __forceinline__ void cvt_dense8(const float* w, int K, int N, unsigned char* dst, LAS float* scr, int gw, int NGW, int lane) {
;     const int nnb = N / 64, items = (K / 64) * nnb;
;     for (int it = gw; it < items; it += NGW) cvt_item8(w, K, N, dst, it / nnb, it % nnb, (it % nnb) * 64, 64.f, scr, lane);
; }
.LBB0_17:
	s_mul_hi_i32 s2, s27, 0x2aaaaaab
	s_lshr_b32 s3, s2, 31
	s_ashr_i32 s2, s2, 2
	s_add_i32 s2, s2, s3
	s_mul_i32 s3, s2, 0xfffffa00
	s_lshl_b32 s2, s2, 6
	s_add_i32 s28, s0, s3
	v_or_b32_e32 v24, s2, v1
	s_movk_i32 s29, 0x1800
	v_mad_i64_i32 v[24:25], s[30:31], v24, s29, v[22:23]
	s_ashr_i32 s29, s28, 31
	s_ashr_i32 s3, s2, 31
	v_lshl_add_u64 v[24:25], s[28:29], 2, v[24:25]
	v_lshl_add_u64 v[30:31], v[20:21], 0, s[2:3]
	v_lshl_add_u64 v[136:137], v[24:25], 0, v[18:19]
	s_movk_i32 s2, 0x6000
	v_add_co_u32_e32 v78, vcc, s2, v136
	v_add_u32_e32 v26, s28, v32
	s_mov_b64 s[2:3], vcc
	s_mov_b32 s28, 0xc000
	v_add_co_u32_e32 v80, vcc, s28, v136
	v_addc_co_u32_e64 v79, s[2:3], 0, v137, s[2:3]
	s_mov_b64 s[2:3], vcc
	s_mov_b32 s28, 0x12000
	v_add_co_u32_e32 v82, vcc, s28, v136
	v_addc_co_u32_e64 v81, s[2:3], 0, v137, s[2:3]
	s_mov_b64 s[2:3], vcc
	v_add_co_u32_e32 v86, vcc, s9, v136
	v_addc_co_u32_e64 v83, s[2:3], 0, v137, s[2:3]
	s_mov_b64 s[2:3], vcc
	v_add_co_u32_e32 v90, vcc, s10, v136
	v_addc_co_u32_e64 v87, s[2:3], 0, v137, s[2:3]
	s_mov_b64 s[2:3], vcc
	v_add_co_u32_e32 v94, vcc, s11, v136
	v_addc_co_u32_e64 v91, s[2:3], 0, v137, s[2:3]
	s_mov_b64 s[2:3], vcc
	v_add_co_u32_e32 v98, vcc, s18, v136
	v_addc_co_u32_e64 v95, s[2:3], 0, v137, s[2:3]
	v_add_u32_e32 v28, 16, v26
	v_add_u32_e32 v74, 32, v26
	v_add_u32_e32 v76, 48, v26
	s_mov_b64 s[2:3], vcc
	v_ashrrev_i32_e32 v27, 31, v26
	v_ashrrev_i32_e32 v29, 31, v28
	v_ashrrev_i32_e32 v75, 31, v74
	v_ashrrev_i32_e32 v77, 31, v76
	v_add_co_u32_e32 v102, vcc, s19, v136
	v_addc_co_u32_e64 v99, s[2:3], 0, v137, s[2:3]
	v_lshlrev_b64 v[24:25], 10, v[26:27]
	global_load_dwordx4 v[70:73], v[136:137], off
	v_lshlrev_b64 v[26:27], 10, v[28:29]
	v_lshlrev_b64 v[28:29], 10, v[74:75]
	v_lshlrev_b64 v[74:75], 10, v[76:77]
	s_mov_b64 s[2:3], vcc
	v_lshl_add_u64 v[24:25], v[30:31], 0, v[24:25]
	v_lshl_add_u64 v[26:27], v[30:31], 0, v[26:27]
	v_lshl_add_u64 v[28:29], v[30:31], 0, v[28:29]
	v_lshl_add_u64 v[30:31], v[30:31], 0, v[74:75]
	global_load_dwordx4 v[74:77], v[78:79], off
	v_add_co_u32_e32 v106, vcc, s20, v136
	v_addc_co_u32_e64 v103, s[2:3], 0, v137, s[2:3]
	global_load_dwordx4 v[82:85], v[82:83], off
	s_mov_b64 s[2:3], vcc
	global_load_dwordx4 v[78:81], v[80:81], off
	v_add_co_u32_e32 v110, vcc, s21, v136
	v_addc_co_u32_e64 v107, s[2:3], 0, v137, s[2:3]
	global_load_dwordx4 v[86:89], v[86:87], off
	s_mov_b64 s[2:3], vcc
	global_load_dwordx4 v[90:93], v[90:91], off
	v_add_co_u32_e32 v114, vcc, s22, v136
	v_addc_co_u32_e64 v111, s[2:3], 0, v137, s[2:3]
	global_load_dwordx4 v[94:97], v[94:95], off
	s_mov_b64 s[2:3], vcc
	global_load_dwordx4 v[98:101], v[98:99], off
	v_add_co_u32_e32 v118, vcc, s23, v136
	v_addc_co_u32_e64 v115, s[2:3], 0, v137, s[2:3]
	global_load_dwordx4 v[102:105], v[102:103], off
	s_mov_b64 s[2:3], vcc
	global_load_dwordx4 v[106:109], v[106:107], off
	v_add_co_u32_e32 v122, vcc, s24, v136
	v_addc_co_u32_e64 v119, s[2:3], 0, v137, s[2:3]
	global_load_dwordx4 v[110:113], v[110:111], off
	s_mov_b64 s[2:3], vcc
	global_load_dwordx4 v[114:117], v[114:115], off
	v_add_co_u32_e32 v126, vcc, s25, v136
	v_addc_co_u32_e64 v123, s[2:3], 0, v137, s[2:3]
	global_load_dwordx4 v[118:121], v[118:119], off
	s_mov_b64 s[2:3], vcc
	global_load_dwordx4 v[122:125], v[122:123], off
	v_add_co_u32_e32 v136, vcc, s26, v136
	v_addc_co_u32_e64 v127, s[2:3], 0, v137, s[2:3]
	global_load_dwordx4 v[126:129], v[126:127], off
	v_addc_co_u32_e32 v137, vcc, 0, v137, vcc
	global_load_dwordx4 v[136:139], v[136:137], off
	v_mov_b32_e32 v2, 0
	v_mov_b32_e32 v3, 0
	v_mov_b32_e32 v4, 0
	v_mov_b32_e32 v5, 0
	v_mov_b32_e32 v6, 0
	v_mov_b32_e32 v7, 0
	v_mov_b32_e32 v8, 0
	v_mov_b32_e32 v9, 0
	v_mov_b32_e32 v10, 0
	v_mov_b32_e32 v11, 0
	v_mov_b32_e32 v12, 0
	v_mov_b32_e32 v13, 0
	v_mov_b32_e32 v14, 0
	v_mov_b32_e32 v15, 0
	v_mov_b32_e32 v16, 0
	v_mov_b32_e32 v17, 0
	s_add_i32 s27, s27, s33
	s_add_i32 s0, s0, s1
	s_cmpk_lt_i32 s27, 0x180
	s_waitcnt vmcnt(15)
	v_pk_mul_f32 v[70:71], v[70:71], s[8:9] op_sel_hi:[1,0]
	v_pk_mul_f32 v[72:73], v[72:73], s[8:9] op_sel_hi:[1,0]
	ds_write2_b32 v35, v70, v71 offset1:1
	ds_write2_b32 v35, v72, v73 offset0:2 offset1:3
	s_waitcnt vmcnt(14)
	v_pk_mul_f32 v[70:71], v[74:75], s[8:9] op_sel_hi:[1,0]
	v_pk_mul_f32 v[72:73], v[76:77], s[8:9] op_sel_hi:[1,0]
	ds_write2_b32 v36, v70, v71 offset1:1
	ds_write2_b32 v37, v72, v73 offset1:1
	s_waitcnt vmcnt(12)
	v_pk_mul_f32 v[70:71], v[78:79], s[8:9] op_sel_hi:[1,0]
	v_pk_mul_f32 v[72:73], v[80:81], s[8:9] op_sel_hi:[1,0]
	ds_write2_b32 v38, v70, v71 offset1:1
	ds_write2_b32 v39, v72, v73 offset1:1
	v_pk_mul_f32 v[70:71], v[82:83], s[8:9] op_sel_hi:[1,0]
	v_pk_mul_f32 v[72:73], v[84:85], s[8:9] op_sel_hi:[1,0]
	ds_write2_b32 v40, v70, v71 offset1:1
	ds_write2_b32 v41, v72, v73 offset1:1
	s_waitcnt vmcnt(11)
	v_pk_mul_f32 v[70:71], v[86:87], s[8:9] op_sel_hi:[1,0]
	v_pk_mul_f32 v[72:73], v[88:89], s[8:9] op_sel_hi:[1,0]
	ds_write2_b32 v42, v70, v71 offset1:1
	ds_write2_b32 v43, v72, v73 offset1:1
	s_waitcnt vmcnt(10)
	v_pk_mul_f32 v[70:71], v[90:91], s[8:9] op_sel_hi:[1,0]
	v_pk_mul_f32 v[72:73], v[92:93], s[8:9] op_sel_hi:[1,0]
	ds_write2_b32 v44, v70, v71 offset1:1
	ds_write2_b32 v45, v72, v73 offset1:1
	s_waitcnt vmcnt(9)
	v_pk_mul_f32 v[70:71], v[94:95], s[8:9] op_sel_hi:[1,0]
	v_pk_mul_f32 v[72:73], v[96:97], s[8:9] op_sel_hi:[1,0]
	ds_write2_b32 v46, v70, v71 offset1:1
	ds_write2_b32 v47, v72, v73 offset1:1
	s_waitcnt vmcnt(8)
; __device__ __forceinline__ unsigned pk4_fp8(float a, float b, float c, float d) { unsigned w = 0u; w = __builtin_amdgcn_cvt_pk_fp8_f32(a, b, w, false); w = __builtin_amdgcn_cvt_pk_fp8_f32(c, d, w, true); return w; }
; #define LAS __attribute__((address_space(3)))
; #define LDS_WAIT() asm volatile("s_waitcnt lgkmcnt(0)" ::: "memory")
; __device__ __forceinline__ void cvt_item8(const float* __restrict__ src, int K, int N, unsigned char* dst, int kb, int nb, int drow0, float wscale, LAS float* scr, int lane) {
;     ...
;     LDS_WAIT();
;     const int c = lane & 3;
; #pragma unroll
;     for (int j = 0; j < 4; ++j) { const int n = (lane >> 2) + 16 * j; const LAS float* q = scr + (16 * c) * 65 + n;
;         v4u o; o.x = pg8::pk4_fp8(q[0], q[65], q[130], q[195]); o.y = pg8::pk4_fp8(q[260], q[325], q[390], q[455]);
;         o.z = pg8::pk4_fp8(q[520], q[585], q[650], q[715]); o.w = pg8::pk4_fp8(q[780], q[845], q[910], q[975]);
;         *(v4u*)(dst + (size_t)(drow0 + n) * K + k0 + 16 * c) = o; }
;     LDS_WAIT();
	v_pk_mul_f32 v[70:71], v[98:99], s[8:9] op_sel_hi:[1,0]
	v_pk_mul_f32 v[72:73], v[100:101], s[8:9] op_sel_hi:[1,0]
	ds_write2_b32 v48, v70, v71 offset1:1
	ds_write2_b32 v49, v72, v73 offset1:1
	s_waitcnt vmcnt(7)
	v_pk_mul_f32 v[70:71], v[102:103], s[8:9] op_sel_hi:[1,0]
	v_pk_mul_f32 v[72:73], v[104:105], s[8:9] op_sel_hi:[1,0]
	ds_write2_b32 v50, v70, v71 offset1:1
	ds_write2_b32 v51, v72, v73 offset1:1
	s_waitcnt vmcnt(6)
	v_pk_mul_f32 v[70:71], v[106:107], s[8:9] op_sel_hi:[1,0]
	v_pk_mul_f32 v[72:73], v[108:109], s[8:9] op_sel_hi:[1,0]
	ds_write2_b32 v52, v70, v71 offset1:1
	ds_write2_b32 v53, v72, v73 offset1:1
	s_waitcnt vmcnt(5)
	v_pk_mul_f32 v[70:71], v[110:111], s[8:9] op_sel_hi:[1,0]
	v_pk_mul_f32 v[72:73], v[112:113], s[8:9] op_sel_hi:[1,0]
	ds_write2_b32 v54, v70, v71 offset1:1
	ds_write2_b32 v55, v72, v73 offset1:1
	s_waitcnt vmcnt(4)
	v_pk_mul_f32 v[70:71], v[114:115], s[8:9] op_sel_hi:[1,0]
	v_pk_mul_f32 v[72:73], v[116:117], s[8:9] op_sel_hi:[1,0]
	ds_write2_b32 v56, v70, v71 offset1:1
	ds_write2_b32 v57, v72, v73 offset1:1
	s_waitcnt vmcnt(3)
	v_pk_mul_f32 v[70:71], v[118:119], s[8:9] op_sel_hi:[1,0]
	v_pk_mul_f32 v[72:73], v[120:121], s[8:9] op_sel_hi:[1,0]
	ds_write2_b32 v58, v70, v71 offset1:1
	ds_write2_b32 v59, v72, v73 offset1:1
	s_waitcnt vmcnt(2)
	v_pk_mul_f32 v[70:71], v[122:123], s[8:9] op_sel_hi:[1,0]
	v_pk_mul_f32 v[72:73], v[124:125], s[8:9] op_sel_hi:[1,0]
	ds_write2_b32 v60, v70, v71 offset1:1
	ds_write2_b32 v61, v72, v73 offset1:1
	s_waitcnt vmcnt(1)
	v_pk_mul_f32 v[70:71], v[126:127], s[8:9] op_sel_hi:[1,0]
	v_pk_mul_f32 v[72:73], v[128:129], s[8:9] op_sel_hi:[1,0]
	ds_write2_b32 v62, v70, v71 offset1:1
	ds_write2_b32 v63, v72, v73 offset1:1
	s_waitcnt vmcnt(0)
	v_pk_mul_f32 v[70:71], v[136:137], s[8:9] op_sel_hi:[1,0]
	v_pk_mul_f32 v[72:73], v[138:139], s[8:9] op_sel_hi:[1,0]
	ds_write2_b32 v64, v70, v71 offset1:1
	ds_write2_b32 v65, v72, v73 offset1:1
	s_waitcnt lgkmcnt(0)
	ds_read2_b32 v[70:71], v34 offset1:16
	ds_read2_b32 v[72:73], v34 offset0:65 offset1:81
	ds_read2_b32 v[74:75], v34 offset0:130 offset1:146
	ds_read2_b32 v[76:77], v34 offset0:195 offset1:211
	ds_read2_b32 v[78:79], v66 offset0:4 offset1:20
	ds_read2_b32 v[80:81], v66 offset0:69 offset1:85
	ds_read2_b32 v[82:83], v66 offset0:134 offset1:150
	ds_read2_b32 v[84:85], v66 offset0:199 offset1:215
	ds_read2_b32 v[86:87], v67 offset0:8 offset1:24
	ds_read2_b32 v[88:89], v67 offset0:73 offset1:89
	ds_read2_b32 v[90:91], v67 offset0:138 offset1:154
	ds_read2_b32 v[92:93], v67 offset0:203 offset1:219
	ds_read2_b32 v[94:95], v68 offset0:12 offset1:28
	ds_read2_b32 v[96:97], v68 offset0:77 offset1:93
	ds_read2_b32 v[98:99], v68 offset0:142 offset1:158
	ds_read2_b32 v[100:101], v68 offset0:207 offset1:223
	ds_read2_b32 v[102:103], v34 offset0:32 offset1:48
	ds_read2_b32 v[104:105], v34 offset0:97 offset1:113
	ds_read2_b32 v[106:107], v34 offset0:162 offset1:178
	ds_read2_b32 v[108:109], v34 offset0:227 offset1:243
	ds_read2_b32 v[110:111], v66 offset0:36 offset1:52
	ds_read2_b32 v[112:113], v66 offset0:101 offset1:117
	ds_read2_b32 v[114:115], v66 offset0:166 offset1:182
	ds_read2_b32 v[116:117], v66 offset0:231 offset1:247
	ds_read2_b32 v[118:119], v67 offset0:40 offset1:56
	ds_read2_b32 v[120:121], v67 offset0:105 offset1:121
	ds_read2_b32 v[122:123], v67 offset0:170 offset1:186
	ds_read2_b32 v[124:125], v67 offset0:235 offset1:251
	ds_read2_b32 v[126:127], v68 offset0:44 offset1:60
	ds_read2_b32 v[128:129], v68 offset0:109 offset1:125
	ds_read2_b32 v[136:137], v68 offset0:174 offset1:190
	ds_read2_b32 v[138:139], v68 offset0:239 offset1:255
	s_waitcnt lgkmcnt(14)
	v_cvt_pk_fp8_f32 v2, v70, v72
	v_cvt_pk_fp8_f32 v3, v78, v80
	v_cvt_pk_fp8_f32 v4, v86, v88
	v_cvt_pk_fp8_f32 v5, v94, v96
	v_cvt_pk_fp8_f32 v6, v71, v73
	v_cvt_pk_fp8_f32 v7, v79, v81
	v_cvt_pk_fp8_f32 v8, v87, v89
	v_cvt_pk_fp8_f32 v9, v95, v97
	v_cvt_pk_fp8_f32 v10, v102, v104
	s_waitcnt lgkmcnt(10)
	v_cvt_pk_fp8_f32 v11, v110, v112
	s_waitcnt lgkmcnt(6)
	v_cvt_pk_fp8_f32 v12, v118, v120
	s_waitcnt lgkmcnt(2)
	v_cvt_pk_fp8_f32 v13, v126, v128
	v_cvt_pk_fp8_f32 v14, v103, v105
	v_cvt_pk_fp8_f32 v15, v111, v113
	v_cvt_pk_fp8_f32 v16, v119, v121
	v_cvt_pk_fp8_f32 v17, v127, v129
	v_cvt_pk_fp8_f32 v2, v74, v76 op_sel:[0,0,1]
	v_cvt_pk_fp8_f32 v3, v82, v84 op_sel:[0,0,1]
	v_cvt_pk_fp8_f32 v4, v90, v92 op_sel:[0,0,1]
	v_cvt_pk_fp8_f32 v5, v98, v100 op_sel:[0,0,1]
	v_cvt_pk_fp8_f32 v6, v75, v77 op_sel:[0,0,1]
	v_cvt_pk_fp8_f32 v7, v83, v85 op_sel:[0,0,1]
	v_cvt_pk_fp8_f32 v8, v91, v93 op_sel:[0,0,1]
	v_cvt_pk_fp8_f32 v9, v99, v101 op_sel:[0,0,1]
	v_cvt_pk_fp8_f32 v10, v106, v108 op_sel:[0,0,1]
	v_cvt_pk_fp8_f32 v11, v114, v116 op_sel:[0,0,1]
	v_cvt_pk_fp8_f32 v12, v122, v124 op_sel:[0,0,1]
	s_waitcnt lgkmcnt(0)
	v_cvt_pk_fp8_f32 v13, v136, v138 op_sel:[0,0,1]
	v_cvt_pk_fp8_f32 v14, v107, v109 op_sel:[0,0,1]
	v_cvt_pk_fp8_f32 v15, v115, v117 op_sel:[0,0,1]
	v_cvt_pk_fp8_f32 v16, v123, v125 op_sel:[0,0,1]
	v_cvt_pk_fp8_f32 v17, v137, v139 op_sel:[0,0,1]
	global_store_dwordx4 v[24:25], v[2:5], off nt
	global_store_dwordx4 v[26:27], v[6:9], off nt
	global_store_dwordx4 v[28:29], v[10:13], off nt
	global_store_dwordx4 v[30:31], v[14:17], off nt
	s_waitcnt lgkmcnt(0)
	s_cbranch_scc1 .LBB0_17

; #define LAS __attribute__((address_space(3)))
; #define LDS_WAIT() asm volatile("s_waitcnt lgkmcnt(0)" ::: "memory")
; __device__ __forceinline__ void cvt_item8(const float* __restrict__ src, int K, int N, unsigned char* dst, int kb, int nb, int drow0, float wscale, LAS float* scr, int lane) {
;     const int k0 = kb * 64, n0 = nb * 64;
;     const float* s = src + (size_t)(k0 + (lane >> 4)) * N + n0 + 4 * (lane & 15);
;     f32x4 v[16];
; #pragma unroll
;     for (int i = 0; i < 16; ++i) v[i] = *(const f32x4*)(s + (size_t)(4 * i) * N);
; #pragma unroll
;     for (int i = 0; i < 16; ++i) { LAS float* p = scr + (4 * i + (lane >> 4)) * 65 + 4 * (lane & 15); p[0] = v[i].x * wscale; p[1] = v[i].y * wscale; p[2] = v[i].z * wscale; p[3] = v[i].w * wscale; }
;     LDS_WAIT();
; __device__ __forceinline__ void cvt_dense8(const float* w, int K, int N, unsigned char* dst, LAS float* scr, int gw, int NGW, int lane) {
;     const int nnb = N / 64, items = (K / 64) * nnb;
;     for (int it = gw; it < items; it += NGW) cvt_item8(w, K, N, dst, it / nnb, it % nnb, (it % nnb) * 64, 64.f, scr, lane);
; }
.LBB0_20:
	s_ashr_i32 s27, s26, 31
	s_lshr_b32 s27, s27, 28
	s_add_i32 s27, s26, s27
	s_ashr_i32 s27, s27, 4
	s_lshl_b32 s28, s27, 6
	s_lshl_b32 s29, s27, 10
	v_or_b32_e32 v58, s28, v1
	s_sub_i32 s30, s0, s29
	v_ashrrev_i32_e32 v59, 31, v58
	v_add_u32_e32 v62, s30, v32
	v_lshlrev_b64 v[58:59], 12, v[58:59]
	s_ashr_i32 s29, s28, 31
	s_ashr_i32 s31, s30, 31
	v_ashrrev_i32_e32 v63, 31, v62
	v_add_u32_e32 v64, 16, v62
	v_add_u32_e32 v66, 32, v62
	v_add_u32_e32 v68, 48, v62
	v_lshl_add_u64 v[58:59], s[42:43], 0, v[58:59]
	v_lshl_add_u64 v[60:61], v[20:21], 0, s[28:29]
	v_lshlrev_b64 v[62:63], 10, v[62:63]
	v_ashrrev_i32_e32 v65, 31, v64
	v_ashrrev_i32_e32 v67, 31, v66
	v_ashrrev_i32_e32 v69, 31, v68
	v_lshl_add_u64 v[58:59], s[30:31], 2, v[58:59]
	v_lshl_add_u64 v[122:123], v[60:61], 0, v[62:63]
	v_lshlrev_b64 v[62:63], 10, v[64:65]
	v_lshlrev_b64 v[64:65], 10, v[66:67]
	v_lshlrev_b64 v[66:67], 10, v[68:69]
	v_lshl_add_u64 v[68:69], v[58:59], 0, v[18:19]
	v_lshl_add_u64 v[124:125], v[60:61], 0, v[62:63]
	v_add_co_u32_e32 v62, vcc, s3, v68
	v_lshl_add_u64 v[128:129], v[60:61], 0, v[66:67]
	s_nop 0
	v_addc_co_u32_e32 v63, vcc, 0, v69, vcc
	v_add_co_u32_e32 v66, vcc, s4, v68
	v_lshl_add_u64 v[126:127], v[60:61], 0, v[64:65]
	s_nop 0
	v_addc_co_u32_e32 v67, vcc, 0, v69, vcc
	v_add_co_u32_e32 v70, vcc, s5, v68
	global_load_dwordx4 v[58:61], v[68:69], off
	s_nop 0
	v_addc_co_u32_e32 v71, vcc, 0, v69, vcc
	v_add_co_u32_e32 v74, vcc, s8, v68
	v_mov_b32_e32 v2, 0
	s_nop 0
	v_addc_co_u32_e32 v75, vcc, 0, v69, vcc
	v_add_co_u32_e32 v78, vcc, s9, v68
	v_mov_b32_e32 v3, 0
	s_nop 0
	v_addc_co_u32_e32 v79, vcc, 0, v69, vcc
	v_add_co_u32_e32 v82, vcc, s10, v68
	v_mov_b32_e32 v4, 0
	s_nop 0
	v_addc_co_u32_e32 v83, vcc, 0, v69, vcc
	v_add_co_u32_e32 v86, vcc, s11, v68
	v_mov_b32_e32 v5, 0
	s_nop 0
	v_addc_co_u32_e32 v87, vcc, 0, v69, vcc
	v_add_co_u32_e32 v90, vcc, s18, v68
	v_mov_b32_e32 v6, 0
	s_nop 0
	v_addc_co_u32_e32 v91, vcc, 0, v69, vcc
	v_add_co_u32_e32 v94, vcc, s19, v68
	v_mov_b32_e32 v7, 0
	s_nop 0
	v_addc_co_u32_e32 v95, vcc, 0, v69, vcc
	v_add_co_u32_e32 v98, vcc, s20, v68
	v_mov_b32_e32 v8, 0
	s_nop 0
	v_addc_co_u32_e32 v99, vcc, 0, v69, vcc
	v_add_co_u32_e32 v102, vcc, s21, v68
	v_mov_b32_e32 v9, 0
	s_nop 0
	v_addc_co_u32_e32 v103, vcc, 0, v69, vcc
	v_add_co_u32_e32 v106, vcc, s22, v68
	v_mov_b32_e32 v10, 0
	s_nop 0
	v_addc_co_u32_e32 v107, vcc, 0, v69, vcc
	v_add_co_u32_e32 v110, vcc, s23, v68
	v_mov_b32_e32 v11, 0
	s_nop 0
	v_addc_co_u32_e32 v111, vcc, 0, v69, vcc
	v_add_co_u32_e32 v114, vcc, s24, v68
	v_mov_b32_e32 v12, 0
	s_nop 0
	v_addc_co_u32_e32 v115, vcc, 0, v69, vcc
	v_add_co_u32_e32 v118, vcc, s25, v68
	v_mov_b32_e32 v13, 0
	s_nop 0
	v_addc_co_u32_e32 v119, vcc, 0, v69, vcc
	global_load_dwordx4 v[62:65], v[62:63], off
	s_nop 0
	global_load_dwordx4 v[66:69], v[66:67], off
	s_nop 0
	global_load_dwordx4 v[70:73], v[70:71], off
	s_nop 0
	global_load_dwordx4 v[74:77], v[74:75], off
	s_nop 0
	global_load_dwordx4 v[78:81], v[78:79], off
	s_nop 0
	global_load_dwordx4 v[82:85], v[82:83], off
	s_nop 0
	global_load_dwordx4 v[86:89], v[86:87], off
	s_nop 0
	global_load_dwordx4 v[90:93], v[90:91], off
	s_nop 0
	global_load_dwordx4 v[94:97], v[94:95], off
	s_nop 0
	global_load_dwordx4 v[98:101], v[98:99], off
	s_nop 0
	global_load_dwordx4 v[102:105], v[102:103], off
	s_nop 0
	global_load_dwordx4 v[106:109], v[106:107], off
	s_nop 0
	global_load_dwordx4 v[110:113], v[110:111], off
	s_nop 0
	global_load_dwordx4 v[114:117], v[114:115], off
	s_nop 0
	global_load_dwordx4 v[118:121], v[118:119], off
	v_mov_b32_e32 v14, 0
	v_mov_b32_e32 v15, 0
	v_mov_b32_e32 v16, 0
	v_mov_b32_e32 v17, 0
	s_add_i32 s26, s26, s33
	s_add_i32 s0, s0, s1
	s_cmpk_lt_i32 s26, 0x100
	s_waitcnt vmcnt(15)
	v_pk_mul_f32 v[58:59], v[58:59], s[2:3] op_sel_hi:[1,0]
	v_pk_mul_f32 v[60:61], v[60:61], s[2:3] op_sel_hi:[1,0]
	ds_write2_b32 v23, v58, v59 offset1:1
	ds_write2_b32 v23, v60, v61 offset0:2 offset1:3
	s_waitcnt vmcnt(14)
	v_pk_mul_f32 v[58:59], v[62:63], s[2:3] op_sel_hi:[1,0]
	v_pk_mul_f32 v[60:61], v[64:65], s[2:3] op_sel_hi:[1,0]
	s_waitcnt vmcnt(13)
	v_pk_mul_f32 v[62:63], v[66:67], s[2:3] op_sel_hi:[1,0]
	v_pk_mul_f32 v[64:65], v[68:69], s[2:3] op_sel_hi:[1,0]
	s_waitcnt vmcnt(12)
	v_pk_mul_f32 v[66:67], v[70:71], s[2:3] op_sel_hi:[1,0]
	v_pk_mul_f32 v[68:69], v[72:73], s[2:3] op_sel_hi:[1,0]
	s_waitcnt vmcnt(11)
	v_pk_mul_f32 v[70:71], v[74:75], s[2:3] op_sel_hi:[1,0]
	v_pk_mul_f32 v[72:73], v[76:77], s[2:3] op_sel_hi:[1,0]
	s_waitcnt vmcnt(10)
	v_pk_mul_f32 v[74:75], v[78:79], s[2:3] op_sel_hi:[1,0]
	v_pk_mul_f32 v[76:77], v[80:81], s[2:3] op_sel_hi:[1,0]
	s_waitcnt vmcnt(9)
	v_pk_mul_f32 v[78:79], v[82:83], s[2:3] op_sel_hi:[1,0]
	v_pk_mul_f32 v[80:81], v[84:85], s[2:3] op_sel_hi:[1,0]
	s_waitcnt vmcnt(8)
	v_pk_mul_f32 v[82:83], v[86:87], s[2:3] op_sel_hi:[1,0]
	v_pk_mul_f32 v[84:85], v[88:89], s[2:3] op_sel_hi:[1,0]
	s_waitcnt vmcnt(7)
	v_pk_mul_f32 v[86:87], v[90:91], s[2:3] op_sel_hi:[1,0]
	v_pk_mul_f32 v[88:89], v[92:93], s[2:3] op_sel_hi:[1,0]
	s_waitcnt vmcnt(6)
	v_pk_mul_f32 v[90:91], v[94:95], s[2:3] op_sel_hi:[1,0]
	v_pk_mul_f32 v[92:93], v[96:97], s[2:3] op_sel_hi:[1,0]
	s_waitcnt vmcnt(5)
	v_pk_mul_f32 v[94:95], v[98:99], s[2:3] op_sel_hi:[1,0]
	v_pk_mul_f32 v[96:97], v[100:101], s[2:3] op_sel_hi:[1,0]
	s_waitcnt vmcnt(4)
; __device__ __forceinline__ unsigned pk4_fp8(float a, float b, float c, float d) { unsigned w = 0u; w = __builtin_amdgcn_cvt_pk_fp8_f32(a, b, w, false); w = __builtin_amdgcn_cvt_pk_fp8_f32(c, d, w, true); return w; }
; #define LAS __attribute__((address_space(3)))
; #define LDS_WAIT() asm volatile("s_waitcnt lgkmcnt(0)" ::: "memory")
; __device__ __forceinline__ void cvt_item8(const float* __restrict__ src, int K, int N, unsigned char* dst, int kb, int nb, int drow0, float wscale, LAS float* scr, int lane) {
;     ...
;     LDS_WAIT();
;     const int c = lane & 3;
; #pragma unroll
;     for (int j = 0; j < 4; ++j) { const int n = (lane >> 2) + 16 * j; const LAS float* q = scr + (16 * c) * 65 + n;
;         v4u o; o.x = pg8::pk4_fp8(q[0], q[65], q[130], q[195]); o.y = pg8::pk4_fp8(q[260], q[325], q[390], q[455]);
;         o.z = pg8::pk4_fp8(q[520], q[585], q[650], q[715]); o.w = pg8::pk4_fp8(q[780], q[845], q[910], q[975]);
;         *(v4u*)(dst + (size_t)(drow0 + n) * K + k0 + 16 * c) = o; }
;     LDS_WAIT();
	v_pk_mul_f32 v[98:99], v[102:103], s[2:3] op_sel_hi:[1,0]
	v_pk_mul_f32 v[100:101], v[104:105], s[2:3] op_sel_hi:[1,0]
	s_waitcnt vmcnt(3)
	v_pk_mul_f32 v[102:103], v[106:107], s[2:3] op_sel_hi:[1,0]
	v_pk_mul_f32 v[104:105], v[108:109], s[2:3] op_sel_hi:[1,0]
	s_waitcnt vmcnt(2)
	v_pk_mul_f32 v[106:107], v[110:111], s[2:3] op_sel_hi:[1,0]
	v_pk_mul_f32 v[108:109], v[112:113], s[2:3] op_sel_hi:[1,0]
	s_waitcnt vmcnt(1)
	v_pk_mul_f32 v[110:111], v[114:115], s[2:3] op_sel_hi:[1,0]
	v_pk_mul_f32 v[112:113], v[116:117], s[2:3] op_sel_hi:[1,0]
	s_waitcnt vmcnt(0)
	v_pk_mul_f32 v[114:115], v[118:119], s[2:3] op_sel_hi:[1,0]
	v_pk_mul_f32 v[116:117], v[120:121], s[2:3] op_sel_hi:[1,0]
	ds_write2_b32 v24, v58, v59 offset1:1
	ds_write2_b32 v25, v60, v61 offset1:1
	ds_write2_b32 v26, v62, v63 offset1:1
	ds_write2_b32 v27, v64, v65 offset1:1
	ds_write2_b32 v28, v66, v67 offset1:1
	ds_write2_b32 v29, v68, v69 offset1:1
	ds_write2_b32 v30, v70, v71 offset1:1
	ds_write2_b32 v31, v72, v73 offset1:1
	ds_write2_b32 v33, v74, v75 offset1:1
	ds_write2_b32 v34, v76, v77 offset1:1
	ds_write2_b32 v35, v78, v79 offset1:1
	ds_write2_b32 v36, v80, v81 offset1:1
	ds_write2_b32 v37, v82, v83 offset1:1
	ds_write2_b32 v38, v84, v85 offset1:1
	ds_write2_b32 v39, v86, v87 offset1:1
	ds_write2_b32 v40, v88, v89 offset1:1
	ds_write2_b32 v41, v90, v91 offset1:1
	ds_write2_b32 v42, v92, v93 offset1:1
	ds_write2_b32 v43, v94, v95 offset1:1
	ds_write2_b32 v44, v96, v97 offset1:1
	ds_write2_b32 v45, v98, v99 offset1:1
	ds_write2_b32 v46, v100, v101 offset1:1
	ds_write2_b32 v47, v102, v103 offset1:1
	ds_write2_b32 v48, v104, v105 offset1:1
	ds_write2_b32 v49, v106, v107 offset1:1
	ds_write2_b32 v50, v108, v109 offset1:1
	ds_write2_b32 v51, v110, v111 offset1:1
	ds_write2_b32 v52, v112, v113 offset1:1
	ds_write2_b32 v53, v114, v115 offset1:1
	ds_write2_b32 v54, v116, v117 offset1:1
	s_waitcnt lgkmcnt(0)
	ds_read2_b32 v[58:59], v22 offset1:16
	ds_read2_b32 v[60:61], v22 offset0:65 offset1:81
	ds_read2_b32 v[62:63], v22 offset0:130 offset1:146
	ds_read2_b32 v[64:65], v22 offset0:195 offset1:211
	ds_read2_b32 v[66:67], v55 offset0:4 offset1:20
	ds_read2_b32 v[68:69], v55 offset0:69 offset1:85
	ds_read2_b32 v[70:71], v55 offset0:134 offset1:150
	ds_read2_b32 v[72:73], v55 offset0:199 offset1:215
	ds_read2_b32 v[74:75], v56 offset0:8 offset1:24
	ds_read2_b32 v[76:77], v56 offset0:73 offset1:89
	ds_read2_b32 v[78:79], v56 offset0:138 offset1:154
	ds_read2_b32 v[80:81], v56 offset0:203 offset1:219
	ds_read2_b32 v[82:83], v57 offset0:12 offset1:28
	ds_read2_b32 v[84:85], v57 offset0:77 offset1:93
	ds_read2_b32 v[86:87], v57 offset0:142 offset1:158
	ds_read2_b32 v[88:89], v57 offset0:207 offset1:223
	ds_read2_b32 v[90:91], v22 offset0:32 offset1:48
	ds_read2_b32 v[92:93], v22 offset0:97 offset1:113
	ds_read2_b32 v[94:95], v22 offset0:162 offset1:178
	ds_read2_b32 v[96:97], v22 offset0:227 offset1:243
	ds_read2_b32 v[98:99], v55 offset0:36 offset1:52
	ds_read2_b32 v[100:101], v55 offset0:101 offset1:117
	ds_read2_b32 v[102:103], v55 offset0:166 offset1:182
	ds_read2_b32 v[104:105], v55 offset0:231 offset1:247
	ds_read2_b32 v[106:107], v56 offset0:40 offset1:56
	ds_read2_b32 v[108:109], v56 offset0:105 offset1:121
	ds_read2_b32 v[110:111], v56 offset0:170 offset1:186
	ds_read2_b32 v[112:113], v56 offset0:235 offset1:251
	ds_read2_b32 v[114:115], v57 offset0:44 offset1:60
	ds_read2_b32 v[116:117], v57 offset0:109 offset1:125
	ds_read2_b32 v[118:119], v57 offset0:174 offset1:190
	ds_read2_b32 v[120:121], v57 offset0:239 offset1:255
	s_waitcnt lgkmcnt(14)
	v_cvt_pk_fp8_f32 v2, v58, v60
	v_cvt_pk_fp8_f32 v3, v66, v68
	v_cvt_pk_fp8_f32 v4, v74, v76
	v_cvt_pk_fp8_f32 v5, v82, v84
	v_cvt_pk_fp8_f32 v6, v59, v61
	v_cvt_pk_fp8_f32 v7, v67, v69
	v_cvt_pk_fp8_f32 v8, v75, v77
	v_cvt_pk_fp8_f32 v9, v83, v85
	v_cvt_pk_fp8_f32 v10, v90, v92
	s_waitcnt lgkmcnt(10)
	v_cvt_pk_fp8_f32 v11, v98, v100
	s_waitcnt lgkmcnt(6)
	v_cvt_pk_fp8_f32 v12, v106, v108
	s_waitcnt lgkmcnt(2)
	v_cvt_pk_fp8_f32 v13, v114, v116
	v_cvt_pk_fp8_f32 v14, v91, v93
	v_cvt_pk_fp8_f32 v15, v99, v101
	v_cvt_pk_fp8_f32 v16, v107, v109
	v_cvt_pk_fp8_f32 v17, v115, v117
	v_cvt_pk_fp8_f32 v2, v62, v64 op_sel:[0,0,1]
	v_cvt_pk_fp8_f32 v3, v70, v72 op_sel:[0,0,1]
	v_cvt_pk_fp8_f32 v4, v78, v80 op_sel:[0,0,1]
	v_cvt_pk_fp8_f32 v5, v86, v88 op_sel:[0,0,1]
	v_cvt_pk_fp8_f32 v6, v63, v65 op_sel:[0,0,1]
	v_cvt_pk_fp8_f32 v7, v71, v73 op_sel:[0,0,1]
	v_cvt_pk_fp8_f32 v8, v79, v81 op_sel:[0,0,1]
	v_cvt_pk_fp8_f32 v9, v87, v89 op_sel:[0,0,1]
	v_cvt_pk_fp8_f32 v10, v94, v96 op_sel:[0,0,1]
	v_cvt_pk_fp8_f32 v11, v102, v104 op_sel:[0,0,1]
	v_cvt_pk_fp8_f32 v12, v110, v112 op_sel:[0,0,1]
	s_waitcnt lgkmcnt(0)
	v_cvt_pk_fp8_f32 v13, v118, v120 op_sel:[0,0,1]
	v_cvt_pk_fp8_f32 v14, v95, v97 op_sel:[0,0,1]
	v_cvt_pk_fp8_f32 v15, v103, v105 op_sel:[0,0,1]
	v_cvt_pk_fp8_f32 v16, v111, v113 op_sel:[0,0,1]
	v_cvt_pk_fp8_f32 v17, v119, v121 op_sel:[0,0,1]
	global_store_dwordx4 v[122:123], v[2:5], off nt
	global_store_dwordx4 v[124:125], v[6:9], off nt
	global_store_dwordx4 v[126:127], v[10:13], off nt
	global_store_dwordx4 v[128:129], v[14:17], off nt
	s_waitcnt lgkmcnt(0)
	s_cbranch_scc1 .LBB0_20

; __device__ __forceinline__ unsigned pk4_fp8(float a, float b, float c, float d) { unsigned w = 0u; w = __builtin_amdgcn_cvt_pk_fp8_f32(a, b, w, false); w = __builtin_amdgcn_cvt_pk_fp8_f32(c, d, w, true); return w; }
; #define LAS __attribute__((address_space(3)))
; #define LDS_WAIT() asm volatile("s_waitcnt lgkmcnt(0)" ::: "memory")
; __device__ __forceinline__ void cvt_pack8(const f32x4 (&v)[16], const CvtItem& c, LAS unsigned char* blk, int s4, int lane) {
;     const float w = c.wscale; const int cb = lane & 15, j = 4 * s4 + (lane >> 4);
; #pragma unroll
;     for (int jn = 0; jn < 4; ++jn) {
;         v4u o; o.x = pg8::pk4_fp8(v[0][jn] * w, v[1][jn] * w, v[2][jn] * w, v[3][jn] * w); o.y = pg8::pk4_fp8(v[4][jn] * w, v[5][jn] * w, v[6][jn] * w, v[7][jn] * w);
;         o.z = pg8::pk4_fp8(v[8][jn] * w, v[9][jn] * w, v[10][jn] * w, v[11][jn] * w); o.w = pg8::pk4_fp8(v[12][jn] * w, v[13][jn] * w, v[14][jn] * w, v[15][jn] * w);
;         *(LAS v4u*)(blk + (4 * cb + jn) * 256 + ((j ^ cb) * 16)) = o; }
; }
; __device__ __forceinline__ void cvt_flush8(const CvtItem& c, const LAS unsigned char* blk, int lane) {
;     LDS_WAIT();
; #pragma unroll
;     for (int t = 0; t < 16; ++t) { const int idx = 64 * t + lane, n = idx >> 4, pc = idx & 15, nn = c.nb * 64 + n;
;         const size_t row = (c.which < 2) ? (size_t)((nn >> 7) * 256 + (nn & 127) + c.which * 128) : (size_t)nn;
;         *(v4u*)(c.dst + row * c.K + 16 * pc) = *(const LAS v4u*)(blk + n * 256 + ((pc ^ ((n >> 2) & 15)) * 16)); }
;     LDS_WAIT();
; }
.LBB0_25:
	s_waitcnt vmcnt(15)
	v_mul_f32_e32 v110, v200, v110
	s_waitcnt vmcnt(14)
	v_mul_f32_e32 v118, v200, v118
	v_mov_b32_e32 v202, v143
	s_waitcnt vmcnt(11)
	v_mul_f32_e32 v98, v200, v98
	s_waitcnt vmcnt(10)
	v_mul_f32_e32 v102, v200, v102
	v_mov_b32_e32 v203, v143
	s_waitcnt vmcnt(7)
	v_mul_f32_e32 v78, v200, v78
	s_waitcnt vmcnt(6)
	v_mul_f32_e32 v86, v200, v86
	v_mov_b32_e32 v204, v143
	s_waitcnt vmcnt(3)
	v_mul_f32_e32 v66, v200, v66
	s_waitcnt vmcnt(2)
	v_mul_f32_e32 v70, v200, v70
	v_mov_b32_e32 v205, v143
	v_cvt_pk_fp8_f32 v202, v110, v118
	v_cvt_pk_fp8_f32 v203, v98, v102
	v_cvt_pk_fp8_f32 v204, v78, v86
	v_cvt_pk_fp8_f32 v205, v66, v70
	v_mul_f32_e32 v122, v200, v122
	v_mul_f32_e32 v126, v200, v126
	v_mul_f32_e32 v106, v200, v106
	v_mul_f32_e32 v110, v200, v114
	v_mul_f32_e32 v90, v200, v90
	v_mul_f32_e32 v94, v200, v94
	s_waitcnt vmcnt(1)
	v_mul_f32_e32 v74, v200, v74
	s_waitcnt vmcnt(0)
	v_mul_f32_e32 v78, v200, v82
	v_cvt_pk_fp8_f32 v202, v122, v126 op_sel:[0,0,1]
	v_cvt_pk_fp8_f32 v203, v106, v110 op_sel:[0,0,1]
	v_cvt_pk_fp8_f32 v204, v90, v94 op_sel:[0,0,1]
	v_cvt_pk_fp8_f32 v205, v74, v78 op_sel:[0,0,1]
	v_mul_f32_e32 v66, v200, v111
	v_mul_f32_e32 v70, v200, v119
	v_mul_f32_e32 v74, v200, v123
	ds_write_b128 v166, v[202:205]
	v_mov_b32_e32 v202, v143
	v_cvt_pk_fp8_f32 v202, v66, v70
	v_mul_f32_e32 v66, v200, v99
	v_mul_f32_e32 v70, v200, v103
	v_mov_b32_e32 v203, v143
	v_cvt_pk_fp8_f32 v203, v66, v70
	v_mul_f32_e32 v66, v200, v79
	v_mul_f32_e32 v70, v200, v87
	v_mov_b32_e32 v204, v143
	v_cvt_pk_fp8_f32 v204, v66, v70
	v_mul_f32_e32 v66, v200, v67
	v_mul_f32_e32 v67, v200, v71
	v_mov_b32_e32 v205, v143
	v_cvt_pk_fp8_f32 v205, v66, v67
	v_mul_f32_e32 v78, v200, v127
	v_cvt_pk_fp8_f32 v202, v74, v78 op_sel:[0,0,1]
	v_mul_f32_e32 v74, v200, v107
	v_mul_f32_e32 v78, v200, v115
	v_cvt_pk_fp8_f32 v203, v74, v78 op_sel:[0,0,1]
	v_mul_f32_e32 v74, v200, v91
	v_mul_f32_e32 v78, v200, v95
	v_mul_f32_e32 v70, v200, v75
	v_mul_f32_e32 v71, v200, v83
	v_cvt_pk_fp8_f32 v204, v74, v78 op_sel:[0,0,1]
	v_cvt_pk_fp8_f32 v205, v70, v71 op_sel:[0,0,1]
	v_mul_f32_e32 v66, v200, v112
	v_mul_f32_e32 v67, v200, v120
	v_mul_f32_e32 v70, v200, v124
	ds_write_b128 v166, v[202:205] offset:256
	v_mov_b32_e32 v202, v143
	v_cvt_pk_fp8_f32 v202, v66, v67
	v_mul_f32_e32 v66, v200, v100
	v_mul_f32_e32 v67, v200, v104
	v_mov_b32_e32 v203, v143
	v_cvt_pk_fp8_f32 v203, v66, v67
	v_mul_f32_e32 v66, v200, v80
	v_mul_f32_e32 v67, v200, v88
	v_mov_b32_e32 v204, v143
	v_cvt_pk_fp8_f32 v204, v66, v67
	v_mul_f32_e32 v66, v200, v68
	v_mul_f32_e32 v67, v200, v72
	v_mov_b32_e32 v205, v143
	v_mul_f32_e32 v71, v200, v128
	v_cvt_pk_fp8_f32 v205, v66, v67
	v_cvt_pk_fp8_f32 v202, v70, v71 op_sel:[0,0,1]
	v_mul_f32_e32 v70, v200, v108
	v_mul_f32_e32 v71, v200, v116
	v_cvt_pk_fp8_f32 v203, v70, v71 op_sel:[0,0,1]
	v_mul_f32_e32 v70, v200, v92
	v_mul_f32_e32 v71, v200, v96
	v_cvt_pk_fp8_f32 v204, v70, v71 op_sel:[0,0,1]
	v_mul_f32_e32 v68, v200, v76
	v_mul_f32_e32 v70, v200, v84
	v_cvt_pk_fp8_f32 v205, v68, v70 op_sel:[0,0,1]
	v_mul_f32_e32 v67, v200, v113
	v_mul_f32_e32 v68, v200, v121
	v_mov_b32_e32 v66, v143
	v_cvt_pk_fp8_f32 v66, v67, v68
	v_mul_f32_e32 v70, v200, v125
	v_mul_f32_e32 v71, v200, v129
	v_mul_f32_e32 v68, v200, v101
	v_cvt_pk_fp8_f32 v66, v70, v71 op_sel:[0,0,1]
	v_mul_f32_e32 v70, v200, v105
	v_mov_b32_e32 v67, v143
	v_cvt_pk_fp8_f32 v67, v68, v70
	v_mul_f32_e32 v71, v200, v109
	v_mul_f32_e32 v72, v200, v117
	v_mul_f32_e32 v70, v200, v81
	v_cvt_pk_fp8_f32 v67, v71, v72 op_sel:[0,0,1]
	v_mul_f32_e32 v71, v200, v89
	v_mov_b32_e32 v68, v143
	v_cvt_pk_fp8_f32 v68, v70, v71
	v_mul_f32_e32 v70, v200, v69
	v_mul_f32_e32 v71, v200, v73
	v_mov_b32_e32 v69, v143
	v_cvt_pk_fp8_f32 v69, v70, v71
	v_mul_f32_e32 v72, v200, v93
	v_mul_f32_e32 v74, v200, v97
	v_cvt_pk_fp8_f32 v68, v72, v74 op_sel:[0,0,1]
	v_mul_f32_e32 v72, v200, v77
	v_mul_f32_e32 v73, v200, v85
	v_cvt_pk_fp8_f32 v69, v72, v73 op_sel:[0,0,1]
	s_lshl_b32 s10, s56, 6
	s_cmp_lt_i32 s33, 2
	ds_write_b128 v166, v[202:205] offset:512
	ds_write_b128 v166, v[66:69] offset:768
	s_cselect_b64 vcc, -1, 0
	s_and_b32 s27, s56, 0x1fffffe
	s_waitcnt lgkmcnt(0)
	s_add_i32 s27, s27, s33
	v_bitop3_b32 v67, s10, v183, v1 bitop3:0xc8
	s_lshl_b32 s27, s27, 7
	ds_read_b128 v[68:71], v162
	v_or_b32_e32 v66, s10, v1
	v_or_b32_e32 v67, s27, v67
	v_cndmask_b32_e32 v72, v66, v67, vcc
	v_mov_b64_e32 v[66:67], s[24:25]
	v_mad_i64_i32 v[72:73], s[24:25], v72, s23, v[66:67]
	v_lshl_add_u64 v[72:73], v[72:73], 0, v[136:137]
	s_waitcnt lgkmcnt(0)
	global_store_dwordx4 v[72:73], v[68:71], off nt
	s_mov_b32 s33, s0
	s_mov_b32 s56, s21
	v_bitop3_b32 v69, s10, v184, v133 bitop3:0xc8
	v_or_b32_e32 v68, s10, v133
	v_or_b32_e32 v69, s27, v69
	v_cndmask_b32_e32 v72, v68, v69, vcc
	ds_read_b128 v[68:71], v167
	v_mad_i64_i32 v[72:73], s[24:25], v72, s23, v[66:67]
	v_lshl_add_u64 v[72:73], v[72:73], 0, v[136:137]
	v_mov_b32_e32 v200, v199
	s_waitcnt lgkmcnt(0)
; #define LAS __attribute__((address_space(3)))
; #define LDS_WAIT() asm volatile("s_waitcnt lgkmcnt(0)" ::: "memory")
; __device__ __forceinline__ void cvt_flush8(const CvtItem& c, const LAS unsigned char* blk, int lane) {
;     LDS_WAIT();
; #pragma unroll
;     for (int t = 0; t < 16; ++t) { const int idx = 64 * t + lane, n = idx >> 4, pc = idx & 15, nn = c.nb * 64 + n;
;         const size_t row = (c.which < 2) ? (size_t)((nn >> 7) * 256 + (nn & 127) + c.which * 128) : (size_t)nn;
;         *(v4u*)(c.dst + row * c.K + 16 * pc) = *(const LAS v4u*)(blk + n * 256 + ((pc ^ ((n >> 2) & 15)) * 16)); }
;     LDS_WAIT();
; }
	global_store_dwordx4 v[72:73], v[68:71], off nt
	s_nop 1
	v_bitop3_b32 v69, s10, v185, v135 bitop3:0xc8
	v_or_b32_e32 v68, s10, v135
	v_or_b32_e32 v69, s27, v69
	v_cndmask_b32_e32 v72, v68, v69, vcc
	ds_read_b128 v[68:71], v168
	v_mad_i64_i32 v[72:73], s[24:25], v72, s23, v[66:67]
	v_lshl_add_u64 v[72:73], v[72:73], 0, v[136:137]
	s_waitcnt lgkmcnt(0)
	global_store_dwordx4 v[72:73], v[68:71], off nt
	s_nop 1
	v_bitop3_b32 v69, s10, v186, v148 bitop3:0xc8
	v_or_b32_e32 v68, s10, v148
	v_or_b32_e32 v69, s27, v69
	v_cndmask_b32_e32 v72, v68, v69, vcc
	ds_read_b128 v[68:71], v169
	v_mad_i64_i32 v[72:73], s[24:25], v72, s23, v[66:67]
	v_lshl_add_u64 v[72:73], v[72:73], 0, v[136:137]
	s_waitcnt lgkmcnt(0)
	global_store_dwordx4 v[72:73], v[68:71], off nt
	s_nop 1
	v_bitop3_b32 v69, s10, v187, v150 bitop3:0xc8
	v_or_b32_e32 v68, s10, v150
	v_or_b32_e32 v69, s27, v69
	v_cndmask_b32_e32 v72, v68, v69, vcc
	ds_read_b128 v[68:71], v170
	v_mad_i64_i32 v[72:73], s[24:25], v72, s23, v[66:67]
	v_lshl_add_u64 v[72:73], v[72:73], 0, v[136:137]
	s_waitcnt lgkmcnt(0)
	global_store_dwordx4 v[72:73], v[68:71], off nt
	s_nop 1
	v_bitop3_b32 v69, s10, v188, v151 bitop3:0xc8
	v_or_b32_e32 v68, s10, v151
	v_or_b32_e32 v69, s27, v69
	v_cndmask_b32_e32 v72, v68, v69, vcc
	ds_read_b128 v[68:71], v171
	v_mad_i64_i32 v[72:73], s[24:25], v72, s23, v[66:67]
	v_lshl_add_u64 v[72:73], v[72:73], 0, v[136:137]
	s_waitcnt lgkmcnt(0)
	global_store_dwordx4 v[72:73], v[68:71], off nt
	s_nop 1
	v_bitop3_b32 v69, s10, v189, v152 bitop3:0xc8
	v_or_b32_e32 v68, s10, v152
	v_or_b32_e32 v69, s27, v69
	v_cndmask_b32_e32 v72, v68, v69, vcc
	ds_read_b128 v[68:71], v172
	v_mad_i64_i32 v[72:73], s[24:25], v72, s23, v[66:67]
	v_lshl_add_u64 v[72:73], v[72:73], 0, v[136:137]
	s_waitcnt lgkmcnt(0)
	global_store_dwordx4 v[72:73], v[68:71], off nt
	s_nop 1
	v_bitop3_b32 v69, s10, v190, v153 bitop3:0xc8
	v_or_b32_e32 v68, s10, v153
	v_or_b32_e32 v69, s27, v69
	v_cndmask_b32_e32 v72, v68, v69, vcc
	ds_read_b128 v[68:71], v173
	v_mad_i64_i32 v[72:73], s[24:25], v72, s23, v[66:67]
	v_lshl_add_u64 v[72:73], v[72:73], 0, v[136:137]
	s_waitcnt lgkmcnt(0)
	global_store_dwordx4 v[72:73], v[68:71], off nt
	s_nop 1
	v_bitop3_b32 v69, s10, v191, v154 bitop3:0xc8
	v_or_b32_e32 v68, s10, v154
	v_or_b32_e32 v69, s27, v69
	v_cndmask_b32_e32 v72, v68, v69, vcc
	ds_read_b128 v[68:71], v174
	v_mad_i64_i32 v[72:73], s[24:25], v72, s23, v[66:67]
	v_lshl_add_u64 v[72:73], v[72:73], 0, v[136:137]
	s_waitcnt lgkmcnt(0)
	global_store_dwordx4 v[72:73], v[68:71], off nt
	s_nop 1
	v_bitop3_b32 v69, s10, v192, v155 bitop3:0xc8
	v_or_b32_e32 v68, s10, v155
	v_or_b32_e32 v69, s27, v69
	v_cndmask_b32_e32 v72, v68, v69, vcc
	ds_read_b128 v[68:71], v175
	v_mad_i64_i32 v[72:73], s[24:25], v72, s23, v[66:67]
	v_lshl_add_u64 v[72:73], v[72:73], 0, v[136:137]
	s_waitcnt lgkmcnt(0)
	global_store_dwordx4 v[72:73], v[68:71], off nt
	s_nop 1
	v_bitop3_b32 v69, s10, v193, v156 bitop3:0xc8
	v_or_b32_e32 v68, s10, v156
	v_or_b32_e32 v69, s27, v69
	v_cndmask_b32_e32 v72, v68, v69, vcc
	ds_read_b128 v[68:71], v176
	v_mad_i64_i32 v[72:73], s[24:25], v72, s23, v[66:67]
	v_lshl_add_u64 v[72:73], v[72:73], 0, v[136:137]
	s_waitcnt lgkmcnt(0)
	global_store_dwordx4 v[72:73], v[68:71], off nt
	s_nop 1
	v_bitop3_b32 v69, s10, v194, v157 bitop3:0xc8
	v_or_b32_e32 v68, s10, v157
	v_or_b32_e32 v69, s27, v69
	v_cndmask_b32_e32 v72, v68, v69, vcc
	ds_read_b128 v[68:71], v177
	v_mad_i64_i32 v[72:73], s[24:25], v72, s23, v[66:67]
	v_lshl_add_u64 v[72:73], v[72:73], 0, v[136:137]
	s_waitcnt lgkmcnt(0)
	global_store_dwordx4 v[72:73], v[68:71], off nt
	s_nop 1
	v_bitop3_b32 v69, s10, v195, v158 bitop3:0xc8
	v_or_b32_e32 v68, s10, v158
	v_or_b32_e32 v69, s27, v69
	v_cndmask_b32_e32 v72, v68, v69, vcc
	ds_read_b128 v[68:71], v178
	v_mad_i64_i32 v[72:73], s[24:25], v72, s23, v[66:67]
	v_lshl_add_u64 v[72:73], v[72:73], 0, v[136:137]
	s_waitcnt lgkmcnt(0)
	global_store_dwordx4 v[72:73], v[68:71], off nt
	s_nop 1
	v_bitop3_b32 v69, s10, v196, v159 bitop3:0xc8
	v_or_b32_e32 v68, s10, v159
	v_or_b32_e32 v69, s27, v69
	v_cndmask_b32_e32 v72, v68, v69, vcc
	ds_read_b128 v[68:71], v179
	v_mad_i64_i32 v[72:73], s[24:25], v72, s23, v[66:67]
	v_lshl_add_u64 v[72:73], v[72:73], 0, v[136:137]
	s_waitcnt lgkmcnt(0)
	global_store_dwordx4 v[72:73], v[68:71], off nt
	s_nop 1
	v_bitop3_b32 v69, s10, v197, v160 bitop3:0xc8
	v_or_b32_e32 v68, s10, v160
	v_or_b32_e32 v69, s27, v69
	v_cndmask_b32_e32 v72, v68, v69, vcc
	ds_read_b128 v[68:71], v180
	v_mad_i64_i32 v[72:73], s[24:25], v72, s23, v[66:67]
	v_lshl_add_u64 v[72:73], v[72:73], 0, v[136:137]
	s_waitcnt lgkmcnt(0)
	global_store_dwordx4 v[72:73], v[68:71], off nt
	s_nop 1
	v_bitop3_b32 v69, s10, v198, v161 bitop3:0xc8
	v_or_b32_e32 v68, s10, v161
	v_or_b32_e32 v69, s27, v69
	v_cndmask_b32_e32 v72, v68, v69, vcc
	ds_read_b128 v[68:71], v181
	v_mad_i64_i32 v[66:67], s[24:25], v72, s23, v[66:67]
	v_lshl_add_u64 v[66:67], v[66:67], 0, v[136:137]
	s_andn2_b64 vcc, exec, s[30:31]
	s_waitcnt lgkmcnt(0)
	global_store_dwordx4 v[66:67], v[68:71], off nt
	s_waitcnt lgkmcnt(0)
	s_mov_b64 s[24:25], s[28:29]
	s_mov_b32 s23, s55
	s_cbranch_vccz .LBB0_31

; __device__ __forceinline__ unsigned pk4_fp8(float a, float b, float c, float d) { unsigned w = 0u; w = __builtin_amdgcn_cvt_pk_fp8_f32(a, b, w, false); w = __builtin_amdgcn_cvt_pk_fp8_f32(c, d, w, true); return w; }
; #define LAS __attribute__((address_space(3)))
; #define LDS_WAIT() asm volatile("s_waitcnt lgkmcnt(0)" ::: "memory")
; __device__ __forceinline__ void cvt_pack8(const f32x4 (&v)[16], const CvtItem& c, LAS unsigned char* blk, int s4, int lane) {
;     const float w = c.wscale; const int cb = lane & 15, j = 4 * s4 + (lane >> 4);
; #pragma unroll
;     for (int jn = 0; jn < 4; ++jn) {
;         v4u o; o.x = pg8::pk4_fp8(v[0][jn] * w, v[1][jn] * w, v[2][jn] * w, v[3][jn] * w); o.y = pg8::pk4_fp8(v[4][jn] * w, v[5][jn] * w, v[6][jn] * w, v[7][jn] * w);
;         o.z = pg8::pk4_fp8(v[8][jn] * w, v[9][jn] * w, v[10][jn] * w, v[11][jn] * w); o.w = pg8::pk4_fp8(v[12][jn] * w, v[13][jn] * w, v[14][jn] * w, v[15][jn] * w);
;         *(LAS v4u*)(blk + (4 * cb + jn) * 256 + ((j ^ cb) * 16)) = o; }
; }
; __device__ __forceinline__ void cvt_flush8(const CvtItem& c, const LAS unsigned char* blk, int lane) {
;     LDS_WAIT();
; #pragma unroll
;     for (int t = 0; t < 16; ++t) { const int idx = 64 * t + lane, n = idx >> 4, pc = idx & 15, nn = c.nb * 64 + n;
;         const size_t row = (c.which < 2) ? (size_t)((nn >> 7) * 256 + (nn & 127) + c.which * 128) : (size_t)nn;
;         *(v4u*)(c.dst + row * c.K + 16 * pc) = *(const LAS v4u*)(blk + n * 256 + ((pc ^ ((n >> 2) & 15)) * 16)); }
;     LDS_WAIT();
; }
.LBB0_34:
	s_waitcnt vmcnt(15)
	v_mul_f32_e32 v102, v149, v102
	s_waitcnt vmcnt(14)
	v_mul_f32_e32 v114, v149, v114
	v_mov_b32_e32 v198, v139
	v_cvt_pk_fp8_f32 v198, v102, v114
	s_waitcnt vmcnt(11)
	v_mul_f32_e32 v102, v149, v106
	s_waitcnt vmcnt(10)
	v_mul_f32_e32 v106, v149, v118
	v_mov_b32_e32 v199, v139
	v_cvt_pk_fp8_f32 v199, v102, v106
	s_waitcnt vmcnt(9)
	v_mul_f32_e32 v74, v149, v74
	s_waitcnt vmcnt(8)
	v_mul_f32_e32 v86, v149, v86
	v_mov_b32_e32 v200, v139
	v_cvt_pk_fp8_f32 v199, v74, v86 op_sel:[0,0,1]
	s_waitcnt vmcnt(7)
	v_mul_f32_e32 v74, v149, v78
	s_waitcnt vmcnt(6)
	v_mul_f32_e32 v78, v149, v90
	v_cvt_pk_fp8_f32 v200, v74, v78
	s_waitcnt vmcnt(3)
	v_mul_f32_e32 v74, v149, v82
	s_waitcnt vmcnt(2)
	v_mul_f32_e32 v78, v149, v94
	v_mov_b32_e32 v201, v139
	v_cvt_pk_fp8_f32 v201, v74, v78
	s_waitcnt vmcnt(1)
	v_mul_f32_e32 v66, v149, v66
	s_waitcnt vmcnt(0)
	v_mul_f32_e32 v70, v149, v70
	v_mov_b32_e32 v202, v139
	v_cvt_pk_fp8_f32 v201, v66, v70 op_sel:[0,0,1]
	v_mul_f32_e32 v66, v149, v103
	v_mul_f32_e32 v70, v149, v115
	v_cvt_pk_fp8_f32 v202, v66, v70
	v_mul_f32_e32 v66, v149, v107
	v_mul_f32_e32 v70, v149, v119
	v_mov_b32_e32 v203, v139
	v_cvt_pk_fp8_f32 v203, v66, v70
	v_mul_f32_e32 v66, v149, v75
	v_mul_f32_e32 v70, v149, v87
	v_mov_b32_e32 v204, v139
	v_cvt_pk_fp8_f32 v203, v66, v70 op_sel:[0,0,1]
	v_mul_f32_e32 v66, v149, v79
	v_mul_f32_e32 v70, v149, v91
	v_cvt_pk_fp8_f32 v204, v66, v70
	v_mul_f32_e32 v66, v149, v83
	v_mul_f32_e32 v70, v149, v95
	v_mov_b32_e32 v205, v139
	v_cvt_pk_fp8_f32 v205, v66, v70
	v_mul_f32_e32 v66, v149, v67
	v_mul_f32_e32 v67, v149, v71
	v_mov_b32_e32 v206, v139
	v_cvt_pk_fp8_f32 v205, v66, v67 op_sel:[0,0,1]
	v_mul_f32_e32 v66, v149, v104
	v_mul_f32_e32 v67, v149, v116
	v_cvt_pk_fp8_f32 v206, v66, v67
	v_mul_f32_e32 v66, v149, v108
	v_mul_f32_e32 v67, v149, v120
	v_mov_b32_e32 v207, v139
	v_cvt_pk_fp8_f32 v207, v66, v67
	v_mul_f32_e32 v66, v149, v76
	v_mul_f32_e32 v67, v149, v88
	v_mov_b32_e32 v208, v139
	v_cvt_pk_fp8_f32 v207, v66, v67 op_sel:[0,0,1]
	v_mul_f32_e32 v66, v149, v80
	v_mul_f32_e32 v67, v149, v92
	v_cvt_pk_fp8_f32 v208, v66, v67
	v_mul_f32_e32 v66, v149, v84
	v_mul_f32_e32 v67, v149, v96
	v_mov_b32_e32 v209, v139
	v_cvt_pk_fp8_f32 v209, v66, v67
	v_mul_f32_e32 v74, v149, v123
	v_mul_f32_e32 v78, v149, v127
	v_cvt_pk_fp8_f32 v202, v74, v78 op_sel:[0,0,1]
	v_mul_f32_e32 v74, v149, v99
	v_mul_f32_e32 v75, v149, v111
	v_mul_f32_e32 v66, v149, v68
	v_mul_f32_e32 v67, v149, v72
	v_cvt_pk_fp8_f32 v204, v74, v75 op_sel:[0,0,1]
	v_cvt_pk_fp8_f32 v209, v66, v67 op_sel:[0,0,1]
	v_mul_f32_e32 v66, v149, v105
	v_mul_f32_e32 v67, v149, v117
	v_mov_b32_e32 v74, v139
	v_cvt_pk_fp8_f32 v74, v66, v67
	v_mul_f32_e32 v66, v149, v109
	v_mul_f32_e32 v67, v149, v121
	v_mov_b32_e32 v75, v139
	v_cvt_pk_fp8_f32 v75, v66, v67
	v_mul_f32_e32 v66, v149, v77
	v_mul_f32_e32 v67, v149, v89
	v_mov_b32_e32 v76, v139
	v_cvt_pk_fp8_f32 v75, v66, v67 op_sel:[0,0,1]
	v_mul_f32_e32 v66, v149, v81
	v_mul_f32_e32 v67, v149, v93
	v_cvt_pk_fp8_f32 v76, v66, v67
	v_mul_f32_e32 v66, v149, v85
	v_mul_f32_e32 v67, v149, v97
	v_mov_b32_e32 v77, v139
	v_mul_f32_e32 v122, v149, v122
	v_mul_f32_e32 v126, v149, v126
	v_mul_f32_e32 v86, v149, v98
	v_mul_f32_e32 v90, v149, v110
	v_mul_f32_e32 v70, v149, v124
	v_mul_f32_e32 v71, v149, v128
	v_cvt_pk_fp8_f32 v77, v66, v67
	v_cvt_pk_fp8_f32 v198, v122, v126 op_sel:[0,0,1]
	v_cvt_pk_fp8_f32 v200, v86, v90 op_sel:[0,0,1]
	v_cvt_pk_fp8_f32 v206, v70, v71 op_sel:[0,0,1]
	v_mul_f32_e32 v70, v149, v100
	v_mul_f32_e32 v71, v149, v112
	s_lshl_b32 s2, s40, 6
	v_cvt_pk_fp8_f32 v208, v70, v71 op_sel:[0,0,1]
	v_mul_f32_e32 v68, v149, v125
	v_mul_f32_e32 v70, v149, v129
	s_cmp_lt_i32 s39, 2
	v_cvt_pk_fp8_f32 v74, v68, v70 op_sel:[0,0,1]
	v_mul_f32_e32 v68, v149, v101
	v_mul_f32_e32 v70, v149, v113
	v_mul_f32_e32 v66, v149, v69
	v_mul_f32_e32 v67, v149, v73
	s_cselect_b64 vcc, -1, 0
	s_and_b32 s9, s40, 0x1fffffe
	v_cvt_pk_fp8_f32 v76, v68, v70 op_sel:[0,0,1]
	v_cvt_pk_fp8_f32 v77, v66, v67 op_sel:[0,0,1]
	s_add_i32 s9, s9, s39
	ds_write_b128 v166, v[198:201]
	ds_write_b128 v166, v[202:205] offset:256
	ds_write_b128 v166, v[206:209] offset:512
	ds_write_b128 v166, v[74:77] offset:768
	v_bitop3_b32 v67, s2, v147, v1 bitop3:0xc8
	s_lshl_b32 s9, s9, 7
	s_waitcnt lgkmcnt(0)
	v_or_b32_e32 v66, s2, v1
	v_or_b32_e32 v67, s9, v67
	v_cndmask_b32_e32 v70, v66, v67, vcc
	ds_read_b128 v[66:69], v162
	v_mov_b64_e32 v[74:75], s[4:5]
	v_mad_i64_i32 v[70:71], s[4:5], v70, s38, v[74:75]
	v_lshl_add_u64 v[76:77], v[70:71], 0, v[136:137]
	ds_read_b128 v[70:73], v167
	s_waitcnt lgkmcnt(1)
	global_store_dwordx4 v[76:77], v[66:69], off nt
	s_mov_b32 s39, s0
	s_mov_b32 s40, s24
	v_bitop3_b32 v67, s2, v182, v133 bitop3:0xc8
	v_or_b32_e32 v66, s2, v133
	v_or_b32_e32 v67, s9, v67
	v_cndmask_b32_e32 v66, v66, v67, vcc
	v_mad_i64_i32 v[66:67], s[4:5], v66, s38, v[74:75]
	v_lshl_add_u64 v[66:67], v[66:67], 0, v[136:137]
	s_waitcnt lgkmcnt(0)
; #define LAS __attribute__((address_space(3)))
; #define LDS_WAIT() asm volatile("s_waitcnt lgkmcnt(0)" ::: "memory")
; __device__ __forceinline__ void cvt_flush8(const CvtItem& c, const LAS unsigned char* blk, int lane) {
;     LDS_WAIT();
; #pragma unroll
;     for (int t = 0; t < 16; ++t) { const int idx = 64 * t + lane, n = idx >> 4, pc = idx & 15, nn = c.nb * 64 + n;
;         const size_t row = (c.which < 2) ? (size_t)((nn >> 7) * 256 + (nn & 127) + c.which * 128) : (size_t)nn;
;         *(v4u*)(c.dst + row * c.K + 16 * pc) = *(const LAS v4u*)(blk + n * 256 + ((pc ^ ((n >> 2) & 15)) * 16)); }
;     LDS_WAIT();
; }
	global_store_dwordx4 v[66:67], v[70:73], off nt
	v_bitop3_b32 v67, s2, v183, v135 bitop3:0xc8
	v_or_b32_e32 v66, s2, v135
	v_or_b32_e32 v67, s9, v67
	v_cndmask_b32_e32 v70, v66, v67, vcc
	ds_read_b128 v[66:69], v168
	v_mad_i64_i32 v[70:71], s[4:5], v70, s38, v[74:75]
	v_lshl_add_u64 v[76:77], v[70:71], 0, v[136:137]
	ds_read_b128 v[70:73], v169
	s_waitcnt lgkmcnt(1)
	global_store_dwordx4 v[76:77], v[66:69], off nt
	v_mov_b32_e32 v149, v197
	s_nop 0
	v_bitop3_b32 v67, s2, v184, v148 bitop3:0xc8
	v_or_b32_e32 v66, s2, v148
	v_or_b32_e32 v67, s9, v67
	v_cndmask_b32_e32 v66, v66, v67, vcc
	v_mad_i64_i32 v[66:67], s[4:5], v66, s38, v[74:75]
	v_lshl_add_u64 v[66:67], v[66:67], 0, v[136:137]
	s_waitcnt lgkmcnt(0)
	global_store_dwordx4 v[66:67], v[70:73], off nt
	v_bitop3_b32 v67, s2, v185, v150 bitop3:0xc8
	v_or_b32_e32 v66, s2, v150
	v_or_b32_e32 v67, s9, v67
	v_cndmask_b32_e32 v70, v66, v67, vcc
	ds_read_b128 v[66:69], v170
	v_mad_i64_i32 v[70:71], s[4:5], v70, s38, v[74:75]
	v_lshl_add_u64 v[76:77], v[70:71], 0, v[136:137]
	ds_read_b128 v[70:73], v171
	s_waitcnt lgkmcnt(1)
	global_store_dwordx4 v[76:77], v[66:69], off nt
	s_nop 1
	v_bitop3_b32 v67, s2, v186, v151 bitop3:0xc8
	v_or_b32_e32 v66, s2, v151
	v_or_b32_e32 v67, s9, v67
	v_cndmask_b32_e32 v66, v66, v67, vcc
	v_mad_i64_i32 v[66:67], s[4:5], v66, s38, v[74:75]
	v_lshl_add_u64 v[66:67], v[66:67], 0, v[136:137]
	s_waitcnt lgkmcnt(0)
	global_store_dwordx4 v[66:67], v[70:73], off nt
	v_bitop3_b32 v67, s2, v187, v152 bitop3:0xc8
	v_or_b32_e32 v66, s2, v152
	v_or_b32_e32 v67, s9, v67
	v_cndmask_b32_e32 v70, v66, v67, vcc
	ds_read_b128 v[66:69], v172
	v_mad_i64_i32 v[70:71], s[4:5], v70, s38, v[74:75]
	v_lshl_add_u64 v[76:77], v[70:71], 0, v[136:137]
	ds_read_b128 v[70:73], v173
	s_waitcnt lgkmcnt(1)
	global_store_dwordx4 v[76:77], v[66:69], off nt
	s_nop 1
	v_bitop3_b32 v67, s2, v188, v153 bitop3:0xc8
	v_or_b32_e32 v66, s2, v153
	v_or_b32_e32 v67, s9, v67
	v_cndmask_b32_e32 v66, v66, v67, vcc
	v_mad_i64_i32 v[66:67], s[4:5], v66, s38, v[74:75]
	v_lshl_add_u64 v[66:67], v[66:67], 0, v[136:137]
	s_waitcnt lgkmcnt(0)
	global_store_dwordx4 v[66:67], v[70:73], off nt
	v_bitop3_b32 v67, s2, v189, v154 bitop3:0xc8
	v_or_b32_e32 v66, s2, v154
	v_or_b32_e32 v67, s9, v67
	v_cndmask_b32_e32 v70, v66, v67, vcc
	ds_read_b128 v[66:69], v174
	v_mad_i64_i32 v[70:71], s[4:5], v70, s38, v[74:75]
	v_lshl_add_u64 v[76:77], v[70:71], 0, v[136:137]
	ds_read_b128 v[70:73], v175
	s_waitcnt lgkmcnt(1)
	global_store_dwordx4 v[76:77], v[66:69], off nt
	s_nop 1
	v_bitop3_b32 v67, s2, v190, v155 bitop3:0xc8
	v_or_b32_e32 v66, s2, v155
	v_or_b32_e32 v67, s9, v67
	v_cndmask_b32_e32 v66, v66, v67, vcc
	v_mad_i64_i32 v[66:67], s[4:5], v66, s38, v[74:75]
	v_lshl_add_u64 v[66:67], v[66:67], 0, v[136:137]
	s_waitcnt lgkmcnt(0)
	global_store_dwordx4 v[66:67], v[70:73], off nt
	v_bitop3_b32 v67, s2, v191, v156 bitop3:0xc8
	v_or_b32_e32 v66, s2, v156
	v_or_b32_e32 v67, s9, v67
	v_cndmask_b32_e32 v70, v66, v67, vcc
	ds_read_b128 v[66:69], v176
	v_mad_i64_i32 v[70:71], s[4:5], v70, s38, v[74:75]
	v_lshl_add_u64 v[76:77], v[70:71], 0, v[136:137]
	ds_read_b128 v[70:73], v177
	s_waitcnt lgkmcnt(1)
	global_store_dwordx4 v[76:77], v[66:69], off nt
	s_nop 1
	v_bitop3_b32 v67, s2, v192, v157 bitop3:0xc8
	v_or_b32_e32 v66, s2, v157
	v_or_b32_e32 v67, s9, v67
	v_cndmask_b32_e32 v66, v66, v67, vcc
	v_mad_i64_i32 v[66:67], s[4:5], v66, s38, v[74:75]
	v_lshl_add_u64 v[66:67], v[66:67], 0, v[136:137]
	s_waitcnt lgkmcnt(0)
	global_store_dwordx4 v[66:67], v[70:73], off nt
	v_bitop3_b32 v67, s2, v193, v158 bitop3:0xc8
	v_or_b32_e32 v66, s2, v158
	v_or_b32_e32 v67, s9, v67
	v_cndmask_b32_e32 v70, v66, v67, vcc
	ds_read_b128 v[66:69], v178
	v_mad_i64_i32 v[70:71], s[4:5], v70, s38, v[74:75]
	v_lshl_add_u64 v[76:77], v[70:71], 0, v[136:137]
	ds_read_b128 v[70:73], v179
	s_waitcnt lgkmcnt(1)
	global_store_dwordx4 v[76:77], v[66:69], off nt
	s_nop 1
	v_bitop3_b32 v67, s2, v194, v159 bitop3:0xc8
	v_or_b32_e32 v66, s2, v159
	v_or_b32_e32 v67, s9, v67
	v_cndmask_b32_e32 v66, v66, v67, vcc
	v_mad_i64_i32 v[66:67], s[4:5], v66, s38, v[74:75]
	v_lshl_add_u64 v[66:67], v[66:67], 0, v[136:137]
	s_waitcnt lgkmcnt(0)
	global_store_dwordx4 v[66:67], v[70:73], off nt
	v_bitop3_b32 v67, s2, v195, v160 bitop3:0xc8
	v_or_b32_e32 v66, s2, v160
	v_or_b32_e32 v67, s9, v67
	v_cndmask_b32_e32 v70, v66, v67, vcc
	ds_read_b128 v[66:69], v180
	v_mad_i64_i32 v[70:71], s[4:5], v70, s38, v[74:75]
	v_lshl_add_u64 v[76:77], v[70:71], 0, v[136:137]
	ds_read_b128 v[70:73], v181
	s_waitcnt lgkmcnt(1)
	global_store_dwordx4 v[76:77], v[66:69], off nt
	s_nop 1
	v_bitop3_b32 v67, s2, v196, v161 bitop3:0xc8
	v_or_b32_e32 v66, s2, v161
	v_or_b32_e32 v67, s9, v67
	v_cndmask_b32_e32 v66, v66, v67, vcc
	v_mad_i64_i32 v[66:67], s[4:5], v66, s38, v[74:75]
	v_lshl_add_u64 v[66:67], v[66:67], 0, v[136:137]
	s_waitcnt lgkmcnt(0)
	global_store_dwordx4 v[66:67], v[70:73], off nt
	s_waitcnt lgkmcnt(0)
	s_andn2_b64 vcc, exec, s[18:19]
	s_mov_b64 s[4:5], s[10:11]
	s_mov_b32 s38, s25
	s_cbranch_vccz .LBB0_40

; __device__ __forceinline__ void rope_table(f32x2* tab, int j) {
;     double th = 1.0;
;     for (int k = 0; k < j; ++k) th *= 0.5623413251903491;
;     const double x2 = th * th; double c = 1.0, s = th, tc = 1.0, ts = th;
; #pragma unroll
;     for (int n = 1; n <= 12; ++n) { tc *= -x2 * (1.0 / (double)((2 * n - 1) * (2 * n))); ts *= -x2 * (1.0 / (double)((2 * n) * (2 * n + 1))); c += tc; s += ts; }
;     double cr = 1.0, sr = 0.0;
;     for (int p = 0; p < 128; ++p) { tab[p * 16 + j] = (f32x2){(float)cr, (float)sr}; const double nc = cr * c - sr * s, ns = sr * c + cr * s; cr = nc; sr = ns; }
; }
.LBB0_46:
	v_cvt_f32_f64_e32 v14, v[6:7]
	v_cvt_f32_f64_e32 v15, v[12:13]
	global_store_dwordx2 v[10:11], v[14:15], off nt
	v_mul_f64 v[14:15], v[2:3], v[12:13]
	v_fma_f64 v[14:15], v[4:5], v[6:7], -v[14:15]
	v_mul_f64 v[6:7], v[2:3], v[6:7]
	v_fmac_f64_e32 v[6:7], v[4:5], v[12:13]
	v_cvt_f32_f64_e32 v12, v[14:15]
	v_cvt_f32_f64_e32 v13, v[6:7]
	global_store_dwordx2 v[8:9], v[12:13], off nt
	v_mul_f64 v[12:13], v[2:3], v[6:7]
	v_add_u32_e32 v1, s0, v134
	v_fma_f64 v[12:13], v[4:5], v[14:15], -v[12:13]
	v_mul_f64 v[14:15], v[2:3], v[14:15]
	v_add_u32_e32 v16, 32, v1
	v_fmac_f64_e32 v[14:15], v[4:5], v[6:7]
	v_ashrrev_i32_e32 v17, 31, v16
	v_cvt_f32_f64_e32 v6, v[12:13]
	v_cvt_f32_f64_e32 v7, v[14:15]
	v_lshl_add_u64 v[16:17], v[16:17], 3, s[16:17]
	global_store_dwordx2 v[16:17], v[6:7], off nt
	v_mul_f64 v[6:7], v[2:3], v[14:15]
	v_fma_f64 v[6:7], v[4:5], v[12:13], -v[6:7]
	v_mul_f64 v[12:13], v[2:3], v[12:13]
	v_add_u32_e32 v16, 48, v1
	v_fmac_f64_e32 v[12:13], v[4:5], v[14:15]
	v_ashrrev_i32_e32 v17, 31, v16
	v_cvt_f32_f64_e32 v14, v[6:7]
	v_cvt_f32_f64_e32 v15, v[12:13]
	v_lshl_add_u64 v[16:17], v[16:17], 3, s[16:17]
	global_store_dwordx2 v[16:17], v[14:15], off nt
	v_mul_f64 v[14:15], v[2:3], v[12:13]
	v_fma_f64 v[14:15], v[4:5], v[6:7], -v[14:15]
	v_mul_f64 v[6:7], v[2:3], v[6:7]
	v_add_u32_e32 v16, 64, v1
	v_fmac_f64_e32 v[6:7], v[4:5], v[12:13]
	v_ashrrev_i32_e32 v17, 31, v16
	v_cvt_f32_f64_e32 v12, v[14:15]
	v_cvt_f32_f64_e32 v13, v[6:7]
	v_lshl_add_u64 v[16:17], v[16:17], 3, s[16:17]
	global_store_dwordx2 v[16:17], v[12:13], off nt
	v_mul_f64 v[12:13], v[2:3], v[6:7]
	v_fma_f64 v[12:13], v[4:5], v[14:15], -v[12:13]
	v_mul_f64 v[14:15], v[2:3], v[14:15]
	v_add_u32_e32 v16, 0x50, v1
	v_fmac_f64_e32 v[14:15], v[4:5], v[6:7]
	v_ashrrev_i32_e32 v17, 31, v16
	v_cvt_f32_f64_e32 v6, v[12:13]
	v_cvt_f32_f64_e32 v7, v[14:15]
	v_lshl_add_u64 v[16:17], v[16:17], 3, s[16:17]
	global_store_dwordx2 v[16:17], v[6:7], off nt
	v_mul_f64 v[6:7], v[2:3], v[14:15]
	v_fma_f64 v[6:7], v[4:5], v[12:13], -v[6:7]
	v_mul_f64 v[12:13], v[2:3], v[12:13]
	v_add_u32_e32 v16, 0x60, v1
	v_fmac_f64_e32 v[12:13], v[4:5], v[14:15]
	v_ashrrev_i32_e32 v17, 31, v16
	v_cvt_f32_f64_e32 v14, v[6:7]
	v_cvt_f32_f64_e32 v15, v[12:13]
	v_lshl_add_u64 v[16:17], v[16:17], 3, s[16:17]
	global_store_dwordx2 v[16:17], v[14:15], off nt
	v_mul_f64 v[16:17], v[2:3], v[6:7]
	v_mul_f64 v[14:15], v[2:3], v[12:13]
	v_fmac_f64_e32 v[16:17], v[4:5], v[12:13]
	v_add_u32_e32 v12, 0x70, v1
	v_fma_f64 v[14:15], v[4:5], v[6:7], -v[14:15]
	v_ashrrev_i32_e32 v13, 31, v12
	v_cvt_f32_f64_e32 v6, v[14:15]
	v_cvt_f32_f64_e32 v7, v[16:17]
	v_lshl_add_u64 v[12:13], v[12:13], 3, s[16:17]
	global_store_dwordx2 v[12:13], v[6:7], off nt
	v_mul_f64 v[6:7], v[2:3], v[16:17]
	v_mul_f64 v[12:13], v[2:3], v[14:15]
	s_addk_i32 s0, 0x80
	v_fma_f64 v[6:7], v[4:5], v[14:15], -v[6:7]
	v_fmac_f64_e32 v[12:13], v[4:5], v[16:17]
	v_lshl_add_u64 v[8:9], v[8:9], 0, s[4:5]
	s_cmpk_lg_i32 s0, 0x800
	v_lshl_add_u64 v[10:11], v[10:11], 0, s[4:5]
	s_cbranch_scc1 .LBB0_46
